# static priority raise for waves 4-7 extended to the GEMM unit epilogues (the K-loop per-segment flips unchanged)
# baseline (speedup 1.0000x reference)
.LBB0_127:
	v_mov_b32_e32 v2, v181
	s_lshl_b32 s54, s73, 8
	v_readlane_b32 s100, v252, 5
	s_cmp_ge_u32 s100, 4
	s_cbranch_scc0 .Lepi_prio_0
	s_setprio 1
.Lepi_prio_0:
	s_nop 15
	s_nop 15
	s_add_i32 s54, s54, s68
	v_and_or_b32 v12, v2, 15, s54
	s_lshl_b32 s54, s76, 8
	v_ashrrev_i32_e32 v2, 1, v2
	v_and_b32_e32 v2, -8, v2
	s_or_b32 s54, s54, s69
	v_add_u32_e32 v2, s54, v2
	v_ashrrev_i32_e32 v3, 31, v2
	v_mov_b64_e32 v[6:7], s[44:45]
	s_movk_i32 s56, 0x4800
	v_mad_i64_i32 v[4:5], s[54:55], v12, s56, v[6:7]
	v_lshlrev_b64 v[8:9], 1, v[2:3]
	v_lshl_add_u64 v[10:11], v[4:5], 0, v[8:9]
	v_cvt_pk_bf16_f32 v2, v154, v155
	v_cvt_pk_bf16_f32 v3, v156, v157
	v_cvt_pk_bf16_f32 v4, v158, v159
	v_cvt_pk_bf16_f32 v5, v160, v161
	global_store_dwordx4 v[10:11], v[2:5], off
	s_and_b64 vcc, exec, s[38:39]
	s_mov_b64 s[38:39], -1
	v_cvt_pk_bf16_f32 v2, v150, v151
	v_cvt_pk_bf16_f32 v3, v152, v153
	v_cvt_pk_bf16_f32 v4, v146, v147
	v_cvt_pk_bf16_f32 v5, v148, v149
	global_store_dwordx4 v[10:11], v[2:5], off offset:256
	s_nop 1
	v_or_b32_e32 v2, 16, v12
	v_mad_i64_i32 v[2:3], s[54:55], v2, s56, v[6:7]
	v_lshl_add_u64 v[10:11], v[2:3], 0, v[8:9]
	v_cvt_pk_bf16_f32 v2, v142, v143
	v_cvt_pk_bf16_f32 v3, v144, v145
	v_cvt_pk_bf16_f32 v4, v138, v139
	v_cvt_pk_bf16_f32 v5, v140, v141
	global_store_dwordx4 v[10:11], v[2:5], off
	s_nop 1
	v_cvt_pk_bf16_f32 v2, v134, v135
	v_cvt_pk_bf16_f32 v3, v136, v137
	v_cvt_pk_bf16_f32 v4, v130, v131
	v_cvt_pk_bf16_f32 v5, v132, v133
	global_store_dwordx4 v[10:11], v[2:5], off offset:256
	s_nop 1
	v_or_b32_e32 v2, 32, v12
	v_mad_i64_i32 v[2:3], s[54:55], v2, s56, v[6:7]
	v_lshl_add_u64 v[10:11], v[2:3], 0, v[8:9]
	v_cvt_pk_bf16_f32 v2, v126, v127
	v_cvt_pk_bf16_f32 v3, v128, v129
	v_cvt_pk_bf16_f32 v4, v122, v123
	v_cvt_pk_bf16_f32 v5, v124, v125
	global_store_dwordx4 v[10:11], v[2:5], off
	s_nop 1
	v_cvt_pk_bf16_f32 v2, v118, v119
	v_cvt_pk_bf16_f32 v3, v120, v121
	v_cvt_pk_bf16_f32 v4, v114, v115
	v_cvt_pk_bf16_f32 v5, v116, v117
	global_store_dwordx4 v[10:11], v[2:5], off offset:256
	s_nop 1
	v_or_b32_e32 v2, 48, v12
	v_mad_i64_i32 v[2:3], s[54:55], v2, s56, v[6:7]
	v_lshl_add_u64 v[10:11], v[2:3], 0, v[8:9]
	v_cvt_pk_bf16_f32 v2, v110, v111
	v_cvt_pk_bf16_f32 v3, v112, v113
	v_cvt_pk_bf16_f32 v4, v106, v107
	v_cvt_pk_bf16_f32 v5, v108, v109
	global_store_dwordx4 v[10:11], v[2:5], off
	s_nop 1
	v_cvt_pk_bf16_f32 v2, v102, v103
	v_cvt_pk_bf16_f32 v3, v104, v105
	v_cvt_pk_bf16_f32 v4, v98, v99
	v_cvt_pk_bf16_f32 v5, v100, v101
	global_store_dwordx4 v[10:11], v[2:5], off offset:256
	s_nop 1
	v_add_u32_e32 v2, 0x80, v12
	v_mad_i64_i32 v[2:3], s[54:55], v2, s56, v[6:7]
	v_lshl_add_u64 v[10:11], v[2:3], 0, v[8:9]
	v_cvt_pk_bf16_f32 v2, v94, v95
	v_cvt_pk_bf16_f32 v3, v96, v97
	v_cvt_pk_bf16_f32 v4, v90, v91
	v_cvt_pk_bf16_f32 v5, v92, v93
	global_store_dwordx4 v[10:11], v[2:5], off
	s_nop 1
	v_cvt_pk_bf16_f32 v2, v86, v87
	v_cvt_pk_bf16_f32 v3, v88, v89
	v_cvt_pk_bf16_f32 v4, v82, v83
	v_cvt_pk_bf16_f32 v5, v84, v85
	global_store_dwordx4 v[10:11], v[2:5], off offset:256
	s_nop 1
	v_add_u32_e32 v2, 0x90, v12
	v_mad_i64_i32 v[2:3], s[54:55], v2, s56, v[6:7]
	v_lshl_add_u64 v[10:11], v[2:3], 0, v[8:9]
	v_cvt_pk_bf16_f32 v2, v78, v79
	v_cvt_pk_bf16_f32 v3, v80, v81
	v_cvt_pk_bf16_f32 v4, v74, v75
	v_cvt_pk_bf16_f32 v5, v76, v77
	global_store_dwordx4 v[10:11], v[2:5], off
	s_nop 1
	v_cvt_pk_bf16_f32 v2, v70, v71
	v_cvt_pk_bf16_f32 v3, v72, v73
	v_cvt_pk_bf16_f32 v4, v66, v67
	v_cvt_pk_bf16_f32 v5, v68, v69
	global_store_dwordx4 v[10:11], v[2:5], off offset:256
	s_nop 1
	v_add_u32_e32 v2, 0xa0, v12
	v_mad_i64_i32 v[2:3], s[54:55], v2, s56, v[6:7]
	v_lshl_add_u64 v[10:11], v[2:3], 0, v[8:9]
	v_cvt_pk_bf16_f32 v2, v62, v63
	v_cvt_pk_bf16_f32 v3, v64, v65
	v_cvt_pk_bf16_f32 v4, v58, v59
	v_cvt_pk_bf16_f32 v5, v60, v61
	global_store_dwordx4 v[10:11], v[2:5], off
	s_nop 1
	v_cvt_pk_bf16_f32 v2, v54, v55
	v_cvt_pk_bf16_f32 v3, v56, v57
	v_cvt_pk_bf16_f32 v4, v50, v51
	v_cvt_pk_bf16_f32 v5, v52, v53
	global_store_dwordx4 v[10:11], v[2:5], off offset:256
	s_nop 1
	v_add_u32_e32 v2, 0xb0, v12
	v_mad_i64_i32 v[2:3], s[54:55], v2, s56, v[6:7]
	v_lshl_add_u64 v[6:7], v[2:3], 0, v[8:9]
	v_cvt_pk_bf16_f32 v2, v46, v47
	v_cvt_pk_bf16_f32 v3, v48, v49
	v_cvt_pk_bf16_f32 v4, v42, v43
	v_cvt_pk_bf16_f32 v5, v44, v45
	global_store_dwordx4 v[6:7], v[2:5], off
	s_nop 1
	v_cvt_pk_bf16_f32 v2, v38, v39
	v_cvt_pk_bf16_f32 v3, v40, v41
	v_cvt_pk_bf16_f32 v4, v34, v35
	v_cvt_pk_bf16_f32 v5, v36, v37
	global_store_dwordx4 v[6:7], v[2:5], off offset:256
	s_cbranch_vccnz .LBB0_115
	s_andn2_b64 vcc, exec, s[42:43]
	s_cbranch_vccnz .LBB0_114
	s_barrier
	s_branch .LBB0_114

.LBB0_149:
	v_mul_f32_e32 v3, 0xbfb8aa3b, v158
	v_exp_f32_e32 v7, v3
	v_mul_f32_e32 v8, 0xbfb8aa3b, v159
	v_exp_f32_e32 v8, v8
	v_mul_f32_e32 v9, 0xbfb8aa3b, v160
	v_add_f32_e32 v7, 1.0, v7
	v_rcp_f32_e32 v7, v7
	v_add_f32_e32 v8, 1.0, v8
	v_rcp_f32_e32 v8, v8
	v_exp_f32_e32 v9, v9
	v_mul_f32_e32 v7, 0x437f0000, v7
	v_rndne_f32_e32 v7, v7
	v_mul_f32_e32 v8, 0x437f0000, v8
	v_max_f32_e32 v7, 1.0, v7
	v_rndne_f32_e32 v8, v8
	v_cvt_pk_u8_f32 v7, v7, 0, 0
	v_max_f32_e32 v8, 1.0, v8
	v_cvt_pk_u8_f32 v7, v8, 1, v7
	v_mul_f32_e32 v8, 0xbfb8aa3b, v161
	v_exp_f32_e32 v8, v8
	v_add_f32_e32 v9, 1.0, v9
	v_rcp_f32_e32 v9, v9
	v_mul_f32_e32 v10, 0xbfb8aa3b, v156
	v_add_f32_e32 v8, 1.0, v8
	v_rcp_f32_e32 v8, v8
	v_mul_f32_e32 v9, 0x437f0000, v9
	v_rndne_f32_e32 v9, v9
	v_max_f32_e32 v9, 1.0, v9
	v_mul_f32_e32 v8, 0x437f0000, v8
	v_rndne_f32_e32 v8, v8
	v_cvt_pk_u8_f32 v7, v9, 2, v7
	v_mul_f32_e32 v9, 0xbfb8aa3b, v154
	v_max_f32_e32 v8, 1.0, v8
	v_exp_f32_e32 v9, v9
	v_cvt_pk_u8_f32 v8, v8, 3, v7
	v_mul_f32_e32 v7, 0xbfb8aa3b, v155
	v_exp_f32_e32 v7, v7
	v_add_f32_e32 v9, 1.0, v9
	v_rcp_f32_e32 v9, v9
	v_exp_f32_e32 v10, v10
	v_add_f32_e32 v7, 1.0, v7
	v_rcp_f32_e32 v7, v7
	v_mul_f32_e32 v9, 0x437f0000, v9
	v_rndne_f32_e32 v9, v9
	v_max_f32_e32 v9, 1.0, v9
	v_mul_f32_e32 v7, 0x437f0000, v7
	v_rndne_f32_e32 v7, v7
	v_cvt_pk_u8_f32 v9, v9, 0, 0
	v_max_f32_e32 v7, 1.0, v7
	v_cvt_pk_u8_f32 v7, v7, 1, v9
	v_mul_f32_e32 v9, 0xbfb8aa3b, v157
	v_exp_f32_e32 v9, v9
	v_add_f32_e32 v10, 1.0, v10
	v_rcp_f32_e32 v10, v10
	v_mul_f32_e32 v11, 0xbfb8aa3b, v152
	v_add_f32_e32 v9, 1.0, v9
	v_rcp_f32_e32 v9, v9
	v_mul_f32_e32 v10, 0x437f0000, v10
	v_rndne_f32_e32 v10, v10
	v_max_f32_e32 v10, 1.0, v10
	v_mul_f32_e32 v9, 0x437f0000, v9
	v_rndne_f32_e32 v9, v9
	v_cvt_pk_u8_f32 v7, v10, 2, v7
	v_mul_f32_e32 v10, 0xbfb8aa3b, v150
	v_max_f32_e32 v9, 1.0, v9
	v_exp_f32_e32 v10, v10
	v_cvt_pk_u8_f32 v9, v9, 3, v7
	v_mul_f32_e32 v7, 0xbfb8aa3b, v151
	v_exp_f32_e32 v7, v7
	v_add_f32_e32 v10, 1.0, v10
	v_rcp_f32_e32 v10, v10
	v_exp_f32_e32 v11, v11
	v_add_f32_e32 v7, 1.0, v7
	v_rcp_f32_e32 v7, v7
	v_mul_f32_e32 v10, 0x437f0000, v10
	v_rndne_f32_e32 v10, v10
	v_max_f32_e32 v10, 1.0, v10
	v_mul_f32_e32 v7, 0x437f0000, v7
	v_rndne_f32_e32 v7, v7
	v_cvt_pk_u8_f32 v10, v10, 0, 0
	v_max_f32_e32 v7, 1.0, v7
	v_cvt_pk_u8_f32 v7, v7, 1, v10
	v_mul_f32_e32 v10, 0xbfb8aa3b, v153
	v_exp_f32_e32 v10, v10
	v_add_f32_e32 v11, 1.0, v11
	v_rcp_f32_e32 v11, v11
	v_mul_f32_e32 v14, 0xbfb8aa3b, v148
	v_add_f32_e32 v10, 1.0, v10
	v_rcp_f32_e32 v10, v10
	v_mul_f32_e32 v11, 0x437f0000, v11
	v_rndne_f32_e32 v11, v11
	v_max_f32_e32 v11, 1.0, v11
	v_mul_f32_e32 v10, 0x437f0000, v10
	v_rndne_f32_e32 v10, v10
	v_cvt_pk_u8_f32 v7, v11, 2, v7
	v_mul_f32_e32 v11, 0xbfb8aa3b, v146
	v_max_f32_e32 v10, 1.0, v10
	v_exp_f32_e32 v11, v11
	v_cvt_pk_u8_f32 v10, v10, 3, v7
	v_mul_f32_e32 v7, 0xbfb8aa3b, v147
	v_exp_f32_e32 v7, v7
	v_add_f32_e32 v11, 1.0, v11
	v_exp_f32_e32 v14, v14
	v_rcp_f32_e32 v11, v11
	v_add_f32_e32 v7, 1.0, v7
	v_rcp_f32_e32 v7, v7
	v_add_f32_e32 v14, 1.0, v14
	v_mul_f32_e32 v15, 0xbfb8aa3b, v149
	v_mul_f32_e32 v11, 0x437f0000, v11
	v_rcp_f32_e32 v14, v14
	v_exp_f32_e32 v15, v15
	v_rndne_f32_e32 v11, v11
	v_mul_f32_e32 v7, 0x437f0000, v7
	v_max_f32_e32 v11, 1.0, v11
	v_rndne_f32_e32 v7, v7
	v_cvt_pk_u8_f32 v11, v11, 0, 0
	v_max_f32_e32 v7, 1.0, v7
	v_cvt_pk_u8_f32 v7, v7, 1, v11
	v_mul_f32_e32 v11, 0x437f0000, v14
	v_add_f32_e32 v14, 1.0, v15
	v_rcp_f32_e32 v14, v14
	s_lshl_b32 s12, s12, 8
	v_mov_b32_e32 v2, v181
	s_add_i32 s12, s12, s68
	v_rndne_f32_e32 v11, v11
	v_readlane_b32 s100, v252, 5
	s_cmp_ge_u32 s100, 4
	s_cbranch_scc0 .Lepi_prio_1
	s_setprio 1
.Lepi_prio_1:
	s_nop 15
	s_nop 15
	v_max_f32_e32 v11, 1.0, v11
	v_and_or_b32 v6, v2, 15, s12
	s_lshl_b32 s12, s18, 8
	s_or_b32 s12, s12, s74
	v_and_b32_e32 v2, -16, v2
	v_cvt_pk_u8_f32 v7, v11, 2, v7
	v_mul_f32_e32 v11, 0x437f0000, v14
	v_add_u32_e32 v2, s12, v2
	v_mov_b64_e32 v[4:5], s[46:47]
	s_movk_i32 s12, 0x1800
	v_rndne_f32_e32 v11, v11
	v_ashrrev_i32_e32 v3, 31, v2
	v_mad_i64_i32 v[12:13], s[54:55], v6, s12, v[4:5]
	v_max_f32_e32 v11, 1.0, v11
	v_cvt_pk_u8_f32 v11, v11, 3, v7
	v_lshl_add_u64 v[12:13], v[12:13], 0, v[2:3]
	v_mul_f32_e32 v7, 0xbfb8aa3b, v142
	global_store_dwordx4 v[12:13], v[8:11], off
	v_exp_f32_e32 v7, v7
	v_mul_f32_e32 v14, 0xbfb8aa3b, v132
	v_or_b32_e32 v8, 16, v6
	v_mad_i64_i32 v[12:13], s[54:55], v8, s12, v[4:5]
	v_mul_f32_e32 v8, 0xbfb8aa3b, v143
	v_exp_f32_e32 v8, v8
	v_add_f32_e32 v7, 1.0, v7
	v_rcp_f32_e32 v7, v7
	v_mul_f32_e32 v9, 0xbfb8aa3b, v144
	v_add_f32_e32 v8, 1.0, v8
	v_rcp_f32_e32 v8, v8
	v_mul_f32_e32 v7, 0x437f0000, v7
	v_rndne_f32_e32 v7, v7
	v_max_f32_e32 v7, 1.0, v7
	v_mul_f32_e32 v8, 0x437f0000, v8
	v_rndne_f32_e32 v8, v8
	v_cvt_pk_u8_f32 v7, v7, 0, 0
	v_max_f32_e32 v8, 1.0, v8
	v_exp_f32_e32 v9, v9
	v_cvt_pk_u8_f32 v7, v8, 1, v7
	v_mul_f32_e32 v8, 0xbfb8aa3b, v145
	v_exp_f32_e32 v8, v8
	v_add_f32_e32 v9, 1.0, v9
	v_rcp_f32_e32 v9, v9
	v_mul_f32_e32 v10, 0xbfb8aa3b, v140
	v_add_f32_e32 v8, 1.0, v8
	v_rcp_f32_e32 v8, v8
	v_mul_f32_e32 v9, 0x437f0000, v9
	v_rndne_f32_e32 v9, v9
	v_max_f32_e32 v9, 1.0, v9
	v_mul_f32_e32 v8, 0x437f0000, v8
	v_rndne_f32_e32 v8, v8
	v_cvt_pk_u8_f32 v7, v9, 2, v7
	v_mul_f32_e32 v9, 0xbfb8aa3b, v138
	v_max_f32_e32 v8, 1.0, v8
	v_exp_f32_e32 v9, v9
	v_cvt_pk_u8_f32 v8, v8, 3, v7
	v_mul_f32_e32 v7, 0xbfb8aa3b, v139
	v_exp_f32_e32 v7, v7
	v_add_f32_e32 v9, 1.0, v9
	v_rcp_f32_e32 v9, v9
	v_exp_f32_e32 v10, v10
	v_add_f32_e32 v7, 1.0, v7
	v_rcp_f32_e32 v7, v7
	v_mul_f32_e32 v9, 0x437f0000, v9
	v_rndne_f32_e32 v9, v9
	v_max_f32_e32 v9, 1.0, v9
	v_mul_f32_e32 v7, 0x437f0000, v7
	v_rndne_f32_e32 v7, v7
	v_cvt_pk_u8_f32 v9, v9, 0, 0
	v_max_f32_e32 v7, 1.0, v7
	v_cvt_pk_u8_f32 v7, v7, 1, v9
	v_mul_f32_e32 v9, 0xbfb8aa3b, v141
	v_exp_f32_e32 v9, v9
	v_add_f32_e32 v10, 1.0, v10
	v_rcp_f32_e32 v10, v10
	v_mul_f32_e32 v11, 0xbfb8aa3b, v136
	v_add_f32_e32 v9, 1.0, v9
	v_rcp_f32_e32 v9, v9
	v_mul_f32_e32 v10, 0x437f0000, v10
	v_rndne_f32_e32 v10, v10
	v_max_f32_e32 v10, 1.0, v10
	v_mul_f32_e32 v9, 0x437f0000, v9
	v_rndne_f32_e32 v9, v9
	v_cvt_pk_u8_f32 v7, v10, 2, v7
	v_mul_f32_e32 v10, 0xbfb8aa3b, v134
	v_max_f32_e32 v9, 1.0, v9
	v_exp_f32_e32 v10, v10
	v_cvt_pk_u8_f32 v9, v9, 3, v7
	v_mul_f32_e32 v7, 0xbfb8aa3b, v135
	v_exp_f32_e32 v7, v7
	v_add_f32_e32 v10, 1.0, v10
	v_rcp_f32_e32 v10, v10
	v_exp_f32_e32 v11, v11
	v_add_f32_e32 v7, 1.0, v7
	v_rcp_f32_e32 v7, v7
	v_mul_f32_e32 v10, 0x437f0000, v10
	v_rndne_f32_e32 v10, v10
	v_max_f32_e32 v10, 1.0, v10
	v_mul_f32_e32 v7, 0x437f0000, v7
	v_rndne_f32_e32 v7, v7
	v_cvt_pk_u8_f32 v10, v10, 0, 0
	v_max_f32_e32 v7, 1.0, v7
	v_cvt_pk_u8_f32 v7, v7, 1, v10
	v_mul_f32_e32 v10, 0xbfb8aa3b, v137
	v_exp_f32_e32 v10, v10
	v_add_f32_e32 v11, 1.0, v11
	v_rcp_f32_e32 v11, v11
	v_exp_f32_e32 v14, v14
	v_add_f32_e32 v10, 1.0, v10
	v_rcp_f32_e32 v10, v10
	v_mul_f32_e32 v11, 0x437f0000, v11
	v_rndne_f32_e32 v11, v11
	v_max_f32_e32 v11, 1.0, v11
	v_mul_f32_e32 v10, 0x437f0000, v10
	v_rndne_f32_e32 v10, v10
	v_cvt_pk_u8_f32 v7, v11, 2, v7
	v_mul_f32_e32 v11, 0xbfb8aa3b, v130
	v_max_f32_e32 v10, 1.0, v10
	v_exp_f32_e32 v11, v11
	v_cvt_pk_u8_f32 v10, v10, 3, v7
	v_mul_f32_e32 v7, 0xbfb8aa3b, v131
	v_exp_f32_e32 v7, v7
	v_add_f32_e32 v11, 1.0, v11
	v_rcp_f32_e32 v11, v11
	v_add_f32_e32 v14, 1.0, v14
	v_add_f32_e32 v7, 1.0, v7
	v_rcp_f32_e32 v7, v7
	v_mul_f32_e32 v15, 0xbfb8aa3b, v133
	v_mul_f32_e32 v11, 0x437f0000, v11
	v_rcp_f32_e32 v14, v14
	v_exp_f32_e32 v15, v15
	v_rndne_f32_e32 v11, v11
	v_mul_f32_e32 v7, 0x437f0000, v7
	v_max_f32_e32 v11, 1.0, v11
	v_rndne_f32_e32 v7, v7
	v_cvt_pk_u8_f32 v11, v11, 0, 0
	v_max_f32_e32 v7, 1.0, v7
	v_cvt_pk_u8_f32 v7, v7, 1, v11
	v_mul_f32_e32 v11, 0x437f0000, v14
	v_add_f32_e32 v14, 1.0, v15
	v_rcp_f32_e32 v14, v14
	v_rndne_f32_e32 v11, v11
	v_max_f32_e32 v11, 1.0, v11
	v_cvt_pk_u8_f32 v7, v11, 2, v7
	v_mul_f32_e32 v11, 0x437f0000, v14
	v_rndne_f32_e32 v11, v11
	v_max_f32_e32 v11, 1.0, v11
	v_cvt_pk_u8_f32 v11, v11, 3, v7
	v_lshl_add_u64 v[12:13], v[12:13], 0, v[2:3]
	v_mul_f32_e32 v7, 0xbfb8aa3b, v126
	global_store_dwordx4 v[12:13], v[8:11], off
	v_exp_f32_e32 v7, v7
	v_mul_f32_e32 v14, 0xbfb8aa3b, v116
	v_or_b32_e32 v8, 32, v6
	v_mad_i64_i32 v[12:13], s[54:55], v8, s12, v[4:5]
	v_mul_f32_e32 v8, 0xbfb8aa3b, v127
	v_exp_f32_e32 v8, v8
	v_add_f32_e32 v7, 1.0, v7
	v_rcp_f32_e32 v7, v7
	v_mul_f32_e32 v9, 0xbfb8aa3b, v128
	v_add_f32_e32 v8, 1.0, v8
	v_rcp_f32_e32 v8, v8
	v_mul_f32_e32 v7, 0x437f0000, v7
	v_rndne_f32_e32 v7, v7
	v_max_f32_e32 v7, 1.0, v7
	v_mul_f32_e32 v8, 0x437f0000, v8
	v_rndne_f32_e32 v8, v8
	v_cvt_pk_u8_f32 v7, v7, 0, 0
	v_max_f32_e32 v8, 1.0, v8
	v_exp_f32_e32 v9, v9
	v_cvt_pk_u8_f32 v7, v8, 1, v7
	v_mul_f32_e32 v8, 0xbfb8aa3b, v129
	v_exp_f32_e32 v8, v8
	v_add_f32_e32 v9, 1.0, v9
	v_rcp_f32_e32 v9, v9
	v_mul_f32_e32 v10, 0xbfb8aa3b, v124
	v_add_f32_e32 v8, 1.0, v8
	v_rcp_f32_e32 v8, v8
	v_mul_f32_e32 v9, 0x437f0000, v9
	v_rndne_f32_e32 v9, v9
	v_max_f32_e32 v9, 1.0, v9
	v_mul_f32_e32 v8, 0x437f0000, v8
	v_rndne_f32_e32 v8, v8
	v_cvt_pk_u8_f32 v7, v9, 2, v7
	v_mul_f32_e32 v9, 0xbfb8aa3b, v122
	v_max_f32_e32 v8, 1.0, v8
	v_exp_f32_e32 v9, v9
	v_cvt_pk_u8_f32 v8, v8, 3, v7
	v_mul_f32_e32 v7, 0xbfb8aa3b, v123
	v_exp_f32_e32 v7, v7
	v_add_f32_e32 v9, 1.0, v9
	v_rcp_f32_e32 v9, v9
	v_exp_f32_e32 v10, v10
	v_add_f32_e32 v7, 1.0, v7
	v_rcp_f32_e32 v7, v7
	v_mul_f32_e32 v9, 0x437f0000, v9
	v_rndne_f32_e32 v9, v9
	v_max_f32_e32 v9, 1.0, v9
	v_mul_f32_e32 v7, 0x437f0000, v7
	v_rndne_f32_e32 v7, v7
	v_cvt_pk_u8_f32 v9, v9, 0, 0
	v_max_f32_e32 v7, 1.0, v7
	v_cvt_pk_u8_f32 v7, v7, 1, v9
	v_mul_f32_e32 v9, 0xbfb8aa3b, v125
	v_exp_f32_e32 v9, v9
	v_add_f32_e32 v10, 1.0, v10
	v_rcp_f32_e32 v10, v10
	v_mul_f32_e32 v11, 0xbfb8aa3b, v120
	v_add_f32_e32 v9, 1.0, v9
	v_rcp_f32_e32 v9, v9
	v_mul_f32_e32 v10, 0x437f0000, v10
	v_rndne_f32_e32 v10, v10
	v_max_f32_e32 v10, 1.0, v10
	v_mul_f32_e32 v9, 0x437f0000, v9
	v_rndne_f32_e32 v9, v9
	v_cvt_pk_u8_f32 v7, v10, 2, v7
	v_mul_f32_e32 v10, 0xbfb8aa3b, v118
	v_max_f32_e32 v9, 1.0, v9
	v_exp_f32_e32 v10, v10
	v_cvt_pk_u8_f32 v9, v9, 3, v7
	v_mul_f32_e32 v7, 0xbfb8aa3b, v119
	v_exp_f32_e32 v7, v7
	v_add_f32_e32 v10, 1.0, v10
	v_rcp_f32_e32 v10, v10
	v_exp_f32_e32 v11, v11
	v_add_f32_e32 v7, 1.0, v7
	v_rcp_f32_e32 v7, v7
	v_mul_f32_e32 v10, 0x437f0000, v10
	v_rndne_f32_e32 v10, v10
	v_max_f32_e32 v10, 1.0, v10
	v_mul_f32_e32 v7, 0x437f0000, v7
	v_rndne_f32_e32 v7, v7
	v_cvt_pk_u8_f32 v10, v10, 0, 0
	v_max_f32_e32 v7, 1.0, v7
	v_cvt_pk_u8_f32 v7, v7, 1, v10
	v_mul_f32_e32 v10, 0xbfb8aa3b, v121
	v_exp_f32_e32 v10, v10
	v_add_f32_e32 v11, 1.0, v11
	v_rcp_f32_e32 v11, v11
	v_exp_f32_e32 v14, v14
	v_add_f32_e32 v10, 1.0, v10
	v_rcp_f32_e32 v10, v10
	v_mul_f32_e32 v11, 0x437f0000, v11
	v_rndne_f32_e32 v11, v11
	v_max_f32_e32 v11, 1.0, v11
	v_mul_f32_e32 v10, 0x437f0000, v10
	v_rndne_f32_e32 v10, v10
	v_cvt_pk_u8_f32 v7, v11, 2, v7
	v_mul_f32_e32 v11, 0xbfb8aa3b, v114
	v_max_f32_e32 v10, 1.0, v10
	v_exp_f32_e32 v11, v11
	v_cvt_pk_u8_f32 v10, v10, 3, v7
	v_mul_f32_e32 v7, 0xbfb8aa3b, v115
	v_exp_f32_e32 v7, v7
	v_add_f32_e32 v11, 1.0, v11
	v_rcp_f32_e32 v11, v11
	v_add_f32_e32 v14, 1.0, v14
	v_add_f32_e32 v7, 1.0, v7
	v_rcp_f32_e32 v7, v7
	v_mul_f32_e32 v15, 0xbfb8aa3b, v117
	v_mul_f32_e32 v11, 0x437f0000, v11
	v_rcp_f32_e32 v14, v14
	v_exp_f32_e32 v15, v15
	v_rndne_f32_e32 v11, v11
	v_mul_f32_e32 v7, 0x437f0000, v7
	v_max_f32_e32 v11, 1.0, v11
	v_rndne_f32_e32 v7, v7
	v_cvt_pk_u8_f32 v11, v11, 0, 0
	v_max_f32_e32 v7, 1.0, v7
	v_cvt_pk_u8_f32 v7, v7, 1, v11
	v_mul_f32_e32 v11, 0x437f0000, v14
	v_add_f32_e32 v14, 1.0, v15
	v_rcp_f32_e32 v14, v14
	v_rndne_f32_e32 v11, v11
	v_max_f32_e32 v11, 1.0, v11
	v_cvt_pk_u8_f32 v7, v11, 2, v7
	v_mul_f32_e32 v11, 0x437f0000, v14
	v_rndne_f32_e32 v11, v11
	v_max_f32_e32 v11, 1.0, v11
	v_cvt_pk_u8_f32 v11, v11, 3, v7
	v_lshl_add_u64 v[12:13], v[12:13], 0, v[2:3]
	v_mul_f32_e32 v7, 0xbfb8aa3b, v110
	global_store_dwordx4 v[12:13], v[8:11], off
	v_exp_f32_e32 v7, v7
	v_mul_f32_e32 v14, 0xbfb8aa3b, v100
	v_or_b32_e32 v8, 48, v6
	v_mad_i64_i32 v[12:13], s[54:55], v8, s12, v[4:5]
	v_mul_f32_e32 v8, 0xbfb8aa3b, v111
	v_exp_f32_e32 v8, v8
	v_add_f32_e32 v7, 1.0, v7
	v_rcp_f32_e32 v7, v7
	v_mul_f32_e32 v9, 0xbfb8aa3b, v112
	v_add_f32_e32 v8, 1.0, v8
	v_rcp_f32_e32 v8, v8
	v_mul_f32_e32 v7, 0x437f0000, v7
	v_rndne_f32_e32 v7, v7
	v_max_f32_e32 v7, 1.0, v7
	v_mul_f32_e32 v8, 0x437f0000, v8
	v_rndne_f32_e32 v8, v8
	v_cvt_pk_u8_f32 v7, v7, 0, 0
	v_max_f32_e32 v8, 1.0, v8
	v_exp_f32_e32 v9, v9
	v_cvt_pk_u8_f32 v7, v8, 1, v7
	v_mul_f32_e32 v8, 0xbfb8aa3b, v113
	v_exp_f32_e32 v8, v8
	v_add_f32_e32 v9, 1.0, v9
	v_rcp_f32_e32 v9, v9
	v_mul_f32_e32 v10, 0xbfb8aa3b, v108
	v_add_f32_e32 v8, 1.0, v8
	v_rcp_f32_e32 v8, v8
	v_mul_f32_e32 v9, 0x437f0000, v9
	v_rndne_f32_e32 v9, v9
	v_max_f32_e32 v9, 1.0, v9
	v_mul_f32_e32 v8, 0x437f0000, v8
	v_rndne_f32_e32 v8, v8
	v_cvt_pk_u8_f32 v7, v9, 2, v7
	v_mul_f32_e32 v9, 0xbfb8aa3b, v106
	v_max_f32_e32 v8, 1.0, v8
	v_exp_f32_e32 v9, v9
	v_cvt_pk_u8_f32 v8, v8, 3, v7
	v_mul_f32_e32 v7, 0xbfb8aa3b, v107
	v_exp_f32_e32 v7, v7
	v_add_f32_e32 v9, 1.0, v9
	v_rcp_f32_e32 v9, v9
	v_exp_f32_e32 v10, v10
	v_add_f32_e32 v7, 1.0, v7
	v_rcp_f32_e32 v7, v7
	v_mul_f32_e32 v9, 0x437f0000, v9
	v_rndne_f32_e32 v9, v9
	v_max_f32_e32 v9, 1.0, v9
	v_mul_f32_e32 v7, 0x437f0000, v7
	v_rndne_f32_e32 v7, v7
	v_cvt_pk_u8_f32 v9, v9, 0, 0
	v_max_f32_e32 v7, 1.0, v7
	v_cvt_pk_u8_f32 v7, v7, 1, v9
	v_mul_f32_e32 v9, 0xbfb8aa3b, v109
	v_exp_f32_e32 v9, v9
	v_add_f32_e32 v10, 1.0, v10
	v_rcp_f32_e32 v10, v10
	v_mul_f32_e32 v11, 0xbfb8aa3b, v104
	v_add_f32_e32 v9, 1.0, v9
	v_rcp_f32_e32 v9, v9
	v_mul_f32_e32 v10, 0x437f0000, v10
	v_rndne_f32_e32 v10, v10
	v_max_f32_e32 v10, 1.0, v10
	v_mul_f32_e32 v9, 0x437f0000, v9
	v_rndne_f32_e32 v9, v9
	v_cvt_pk_u8_f32 v7, v10, 2, v7
	v_mul_f32_e32 v10, 0xbfb8aa3b, v102
	v_max_f32_e32 v9, 1.0, v9
	v_exp_f32_e32 v10, v10
	v_cvt_pk_u8_f32 v9, v9, 3, v7
	v_mul_f32_e32 v7, 0xbfb8aa3b, v103
	v_exp_f32_e32 v7, v7
	v_add_f32_e32 v10, 1.0, v10
	v_rcp_f32_e32 v10, v10
	v_exp_f32_e32 v11, v11
	v_add_f32_e32 v7, 1.0, v7
	v_rcp_f32_e32 v7, v7
	v_mul_f32_e32 v10, 0x437f0000, v10
	v_rndne_f32_e32 v10, v10
	v_max_f32_e32 v10, 1.0, v10
	v_mul_f32_e32 v7, 0x437f0000, v7
	v_rndne_f32_e32 v7, v7
	v_cvt_pk_u8_f32 v10, v10, 0, 0
	v_max_f32_e32 v7, 1.0, v7
	v_cvt_pk_u8_f32 v7, v7, 1, v10
	v_mul_f32_e32 v10, 0xbfb8aa3b, v105
	v_exp_f32_e32 v10, v10
	v_add_f32_e32 v11, 1.0, v11
	v_rcp_f32_e32 v11, v11
	v_exp_f32_e32 v14, v14
	v_add_f32_e32 v10, 1.0, v10
	v_rcp_f32_e32 v10, v10
	v_mul_f32_e32 v11, 0x437f0000, v11
	v_rndne_f32_e32 v11, v11
	v_max_f32_e32 v11, 1.0, v11
	v_mul_f32_e32 v10, 0x437f0000, v10
	v_rndne_f32_e32 v10, v10
	v_cvt_pk_u8_f32 v7, v11, 2, v7
	v_mul_f32_e32 v11, 0xbfb8aa3b, v98
	v_max_f32_e32 v10, 1.0, v10
	v_exp_f32_e32 v11, v11
	v_cvt_pk_u8_f32 v10, v10, 3, v7
	v_mul_f32_e32 v7, 0xbfb8aa3b, v99
	v_exp_f32_e32 v7, v7
	v_add_f32_e32 v11, 1.0, v11
	v_rcp_f32_e32 v11, v11
	v_add_f32_e32 v14, 1.0, v14
	v_add_f32_e32 v7, 1.0, v7
	v_rcp_f32_e32 v7, v7
	v_mul_f32_e32 v15, 0xbfb8aa3b, v101
	v_mul_f32_e32 v11, 0x437f0000, v11
	v_rcp_f32_e32 v14, v14
	v_exp_f32_e32 v15, v15
	v_rndne_f32_e32 v11, v11
	v_mul_f32_e32 v7, 0x437f0000, v7
	v_max_f32_e32 v11, 1.0, v11
	v_rndne_f32_e32 v7, v7
	v_cvt_pk_u8_f32 v11, v11, 0, 0
	v_max_f32_e32 v7, 1.0, v7
	v_cvt_pk_u8_f32 v7, v7, 1, v11
	v_mul_f32_e32 v11, 0x437f0000, v14
	v_add_f32_e32 v14, 1.0, v15
	v_rcp_f32_e32 v14, v14
	v_rndne_f32_e32 v11, v11
	v_max_f32_e32 v11, 1.0, v11
	v_cvt_pk_u8_f32 v7, v11, 2, v7
	v_mul_f32_e32 v11, 0x437f0000, v14
	v_rndne_f32_e32 v11, v11
	v_max_f32_e32 v11, 1.0, v11
	v_cvt_pk_u8_f32 v11, v11, 3, v7
	v_lshl_add_u64 v[12:13], v[12:13], 0, v[2:3]
	v_mul_f32_e32 v7, 0xbfb8aa3b, v94
	global_store_dwordx4 v[12:13], v[8:11], off
	v_exp_f32_e32 v7, v7
	v_mul_f32_e32 v14, 0xbfb8aa3b, v84
	v_add_u32_e32 v8, 0x80, v6
	v_mad_i64_i32 v[12:13], s[54:55], v8, s12, v[4:5]
	v_mul_f32_e32 v8, 0xbfb8aa3b, v95
	v_exp_f32_e32 v8, v8
	v_add_f32_e32 v7, 1.0, v7
	v_rcp_f32_e32 v7, v7
	v_mul_f32_e32 v9, 0xbfb8aa3b, v96
	v_add_f32_e32 v8, 1.0, v8
	v_rcp_f32_e32 v8, v8
	v_mul_f32_e32 v7, 0x437f0000, v7
	v_rndne_f32_e32 v7, v7
	v_max_f32_e32 v7, 1.0, v7
	v_mul_f32_e32 v8, 0x437f0000, v8
	v_rndne_f32_e32 v8, v8
	v_cvt_pk_u8_f32 v7, v7, 0, 0
	v_max_f32_e32 v8, 1.0, v8
	v_exp_f32_e32 v9, v9
	v_cvt_pk_u8_f32 v7, v8, 1, v7
	v_mul_f32_e32 v8, 0xbfb8aa3b, v97
	v_exp_f32_e32 v8, v8
	v_add_f32_e32 v9, 1.0, v9
	v_rcp_f32_e32 v9, v9
	v_mul_f32_e32 v10, 0xbfb8aa3b, v92
	v_add_f32_e32 v8, 1.0, v8
	v_rcp_f32_e32 v8, v8
	v_mul_f32_e32 v9, 0x437f0000, v9
	v_rndne_f32_e32 v9, v9
	v_max_f32_e32 v9, 1.0, v9
	v_mul_f32_e32 v8, 0x437f0000, v8
	v_rndne_f32_e32 v8, v8
	v_cvt_pk_u8_f32 v7, v9, 2, v7
	v_mul_f32_e32 v9, 0xbfb8aa3b, v90
	v_max_f32_e32 v8, 1.0, v8
	v_exp_f32_e32 v9, v9
	v_cvt_pk_u8_f32 v8, v8, 3, v7
	v_mul_f32_e32 v7, 0xbfb8aa3b, v91
	v_exp_f32_e32 v7, v7
	v_add_f32_e32 v9, 1.0, v9
	v_rcp_f32_e32 v9, v9
	v_exp_f32_e32 v10, v10
	v_add_f32_e32 v7, 1.0, v7
	v_rcp_f32_e32 v7, v7
	v_mul_f32_e32 v9, 0x437f0000, v9
	v_rndne_f32_e32 v9, v9
	v_max_f32_e32 v9, 1.0, v9
	v_mul_f32_e32 v7, 0x437f0000, v7
	v_rndne_f32_e32 v7, v7
	v_cvt_pk_u8_f32 v9, v9, 0, 0
	v_max_f32_e32 v7, 1.0, v7
	v_cvt_pk_u8_f32 v7, v7, 1, v9
	v_mul_f32_e32 v9, 0xbfb8aa3b, v93
	v_exp_f32_e32 v9, v9
	v_add_f32_e32 v10, 1.0, v10
	v_rcp_f32_e32 v10, v10
	v_mul_f32_e32 v11, 0xbfb8aa3b, v88
	v_add_f32_e32 v9, 1.0, v9
	v_rcp_f32_e32 v9, v9
	v_mul_f32_e32 v10, 0x437f0000, v10
	v_rndne_f32_e32 v10, v10
	v_max_f32_e32 v10, 1.0, v10
	v_mul_f32_e32 v9, 0x437f0000, v9
	v_rndne_f32_e32 v9, v9
	v_cvt_pk_u8_f32 v7, v10, 2, v7
	v_mul_f32_e32 v10, 0xbfb8aa3b, v86
	v_max_f32_e32 v9, 1.0, v9
	v_exp_f32_e32 v10, v10
	v_cvt_pk_u8_f32 v9, v9, 3, v7
	v_mul_f32_e32 v7, 0xbfb8aa3b, v87
	v_exp_f32_e32 v7, v7
	v_add_f32_e32 v10, 1.0, v10
	v_rcp_f32_e32 v10, v10
	v_exp_f32_e32 v11, v11
	v_add_f32_e32 v7, 1.0, v7
	v_rcp_f32_e32 v7, v7
	v_mul_f32_e32 v10, 0x437f0000, v10
	v_rndne_f32_e32 v10, v10
	v_max_f32_e32 v10, 1.0, v10
	v_mul_f32_e32 v7, 0x437f0000, v7
	v_rndne_f32_e32 v7, v7
	v_cvt_pk_u8_f32 v10, v10, 0, 0
	v_max_f32_e32 v7, 1.0, v7
	v_cvt_pk_u8_f32 v7, v7, 1, v10
	v_mul_f32_e32 v10, 0xbfb8aa3b, v89
	v_exp_f32_e32 v10, v10
	v_add_f32_e32 v11, 1.0, v11
	v_rcp_f32_e32 v11, v11
	v_exp_f32_e32 v14, v14
	v_add_f32_e32 v10, 1.0, v10
	v_rcp_f32_e32 v10, v10
	v_mul_f32_e32 v11, 0x437f0000, v11
	v_rndne_f32_e32 v11, v11
	v_max_f32_e32 v11, 1.0, v11
	v_mul_f32_e32 v10, 0x437f0000, v10
	v_rndne_f32_e32 v10, v10
	v_cvt_pk_u8_f32 v7, v11, 2, v7
	v_mul_f32_e32 v11, 0xbfb8aa3b, v82
	v_max_f32_e32 v10, 1.0, v10
	v_exp_f32_e32 v11, v11
	v_cvt_pk_u8_f32 v10, v10, 3, v7
	v_mul_f32_e32 v7, 0xbfb8aa3b, v83
	v_exp_f32_e32 v7, v7
	v_add_f32_e32 v11, 1.0, v11
	v_rcp_f32_e32 v11, v11
	v_add_f32_e32 v14, 1.0, v14
	v_add_f32_e32 v7, 1.0, v7
	v_rcp_f32_e32 v7, v7
	v_mul_f32_e32 v15, 0xbfb8aa3b, v85
	v_mul_f32_e32 v11, 0x437f0000, v11
	v_rcp_f32_e32 v14, v14
	v_exp_f32_e32 v15, v15
	v_rndne_f32_e32 v11, v11
	v_mul_f32_e32 v7, 0x437f0000, v7
	v_max_f32_e32 v11, 1.0, v11
	v_rndne_f32_e32 v7, v7
	v_cvt_pk_u8_f32 v11, v11, 0, 0
	v_max_f32_e32 v7, 1.0, v7
	v_cvt_pk_u8_f32 v7, v7, 1, v11
	v_mul_f32_e32 v11, 0x437f0000, v14
	v_add_f32_e32 v14, 1.0, v15
	v_rcp_f32_e32 v14, v14
	v_rndne_f32_e32 v11, v11
	v_max_f32_e32 v11, 1.0, v11
	v_cvt_pk_u8_f32 v7, v11, 2, v7
	v_mul_f32_e32 v11, 0x437f0000, v14
	v_rndne_f32_e32 v11, v11
	v_max_f32_e32 v11, 1.0, v11
	v_cvt_pk_u8_f32 v11, v11, 3, v7
	v_lshl_add_u64 v[12:13], v[12:13], 0, v[2:3]
	v_mul_f32_e32 v7, 0xbfb8aa3b, v78
	global_store_dwordx4 v[12:13], v[8:11], off
	v_exp_f32_e32 v7, v7
	v_mul_f32_e32 v14, 0xbfb8aa3b, v68
	v_add_u32_e32 v8, 0x90, v6
	v_mad_i64_i32 v[12:13], s[54:55], v8, s12, v[4:5]
	v_mul_f32_e32 v8, 0xbfb8aa3b, v79
	v_exp_f32_e32 v8, v8
	v_add_f32_e32 v7, 1.0, v7
	v_rcp_f32_e32 v7, v7
	v_mul_f32_e32 v9, 0xbfb8aa3b, v80
	v_add_f32_e32 v8, 1.0, v8
	v_rcp_f32_e32 v8, v8
	v_mul_f32_e32 v7, 0x437f0000, v7
	v_rndne_f32_e32 v7, v7
	v_max_f32_e32 v7, 1.0, v7
	v_mul_f32_e32 v8, 0x437f0000, v8
	v_rndne_f32_e32 v8, v8
	v_cvt_pk_u8_f32 v7, v7, 0, 0
	v_max_f32_e32 v8, 1.0, v8
	v_exp_f32_e32 v9, v9
	v_cvt_pk_u8_f32 v7, v8, 1, v7
	v_mul_f32_e32 v8, 0xbfb8aa3b, v81
	v_exp_f32_e32 v8, v8
	v_add_f32_e32 v9, 1.0, v9
	v_rcp_f32_e32 v9, v9
	v_mul_f32_e32 v10, 0xbfb8aa3b, v76
	v_add_f32_e32 v8, 1.0, v8
	v_rcp_f32_e32 v8, v8
	v_mul_f32_e32 v9, 0x437f0000, v9
	v_rndne_f32_e32 v9, v9
	v_max_f32_e32 v9, 1.0, v9
	v_mul_f32_e32 v8, 0x437f0000, v8
	v_rndne_f32_e32 v8, v8
	v_cvt_pk_u8_f32 v7, v9, 2, v7
	v_mul_f32_e32 v9, 0xbfb8aa3b, v74
	v_max_f32_e32 v8, 1.0, v8
	v_exp_f32_e32 v9, v9
	v_cvt_pk_u8_f32 v8, v8, 3, v7
	v_mul_f32_e32 v7, 0xbfb8aa3b, v75
	v_exp_f32_e32 v7, v7
	v_add_f32_e32 v9, 1.0, v9
	v_rcp_f32_e32 v9, v9
	v_exp_f32_e32 v10, v10
	v_add_f32_e32 v7, 1.0, v7
	v_rcp_f32_e32 v7, v7
	v_mul_f32_e32 v9, 0x437f0000, v9
	v_rndne_f32_e32 v9, v9
	v_max_f32_e32 v9, 1.0, v9
	v_mul_f32_e32 v7, 0x437f0000, v7
	v_rndne_f32_e32 v7, v7
	v_cvt_pk_u8_f32 v9, v9, 0, 0
	v_max_f32_e32 v7, 1.0, v7
	v_cvt_pk_u8_f32 v7, v7, 1, v9
	v_mul_f32_e32 v9, 0xbfb8aa3b, v77
	v_exp_f32_e32 v9, v9
	v_add_f32_e32 v10, 1.0, v10
	v_rcp_f32_e32 v10, v10
	v_mul_f32_e32 v11, 0xbfb8aa3b, v72
	v_add_f32_e32 v9, 1.0, v9
	v_rcp_f32_e32 v9, v9
	v_mul_f32_e32 v10, 0x437f0000, v10
	v_rndne_f32_e32 v10, v10
	v_max_f32_e32 v10, 1.0, v10
	v_mul_f32_e32 v9, 0x437f0000, v9
	v_rndne_f32_e32 v9, v9
	v_cvt_pk_u8_f32 v7, v10, 2, v7
	v_mul_f32_e32 v10, 0xbfb8aa3b, v70
	v_max_f32_e32 v9, 1.0, v9
	v_exp_f32_e32 v10, v10
	v_cvt_pk_u8_f32 v9, v9, 3, v7
	v_mul_f32_e32 v7, 0xbfb8aa3b, v71
	v_exp_f32_e32 v7, v7
	v_add_f32_e32 v10, 1.0, v10
	v_rcp_f32_e32 v10, v10
	v_exp_f32_e32 v11, v11
	v_add_f32_e32 v7, 1.0, v7
	v_rcp_f32_e32 v7, v7
	v_mul_f32_e32 v10, 0x437f0000, v10
	v_rndne_f32_e32 v10, v10
	v_max_f32_e32 v10, 1.0, v10
	v_mul_f32_e32 v7, 0x437f0000, v7
	v_rndne_f32_e32 v7, v7
	v_cvt_pk_u8_f32 v10, v10, 0, 0
	v_max_f32_e32 v7, 1.0, v7
	v_cvt_pk_u8_f32 v7, v7, 1, v10
	v_mul_f32_e32 v10, 0xbfb8aa3b, v73
	v_exp_f32_e32 v10, v10
	v_add_f32_e32 v11, 1.0, v11
	v_rcp_f32_e32 v11, v11
	v_exp_f32_e32 v14, v14
	v_add_f32_e32 v10, 1.0, v10
	v_rcp_f32_e32 v10, v10
	v_mul_f32_e32 v11, 0x437f0000, v11
	v_rndne_f32_e32 v11, v11
	v_max_f32_e32 v11, 1.0, v11
	v_mul_f32_e32 v10, 0x437f0000, v10
	v_rndne_f32_e32 v10, v10
	v_cvt_pk_u8_f32 v7, v11, 2, v7
	v_mul_f32_e32 v11, 0xbfb8aa3b, v66
	v_max_f32_e32 v10, 1.0, v10
	v_exp_f32_e32 v11, v11
	v_cvt_pk_u8_f32 v10, v10, 3, v7
	v_mul_f32_e32 v7, 0xbfb8aa3b, v67
	v_exp_f32_e32 v7, v7
	v_add_f32_e32 v11, 1.0, v11
	v_rcp_f32_e32 v11, v11
	v_add_f32_e32 v14, 1.0, v14
	v_add_f32_e32 v7, 1.0, v7
	v_rcp_f32_e32 v7, v7
	v_mul_f32_e32 v15, 0xbfb8aa3b, v69
	v_mul_f32_e32 v11, 0x437f0000, v11
	v_rcp_f32_e32 v14, v14
	v_exp_f32_e32 v15, v15
	v_rndne_f32_e32 v11, v11
	v_mul_f32_e32 v7, 0x437f0000, v7
	v_max_f32_e32 v11, 1.0, v11
	v_rndne_f32_e32 v7, v7
	v_cvt_pk_u8_f32 v11, v11, 0, 0
	v_max_f32_e32 v7, 1.0, v7
	v_cvt_pk_u8_f32 v7, v7, 1, v11
	v_mul_f32_e32 v11, 0x437f0000, v14
	v_add_f32_e32 v14, 1.0, v15
	v_rcp_f32_e32 v14, v14
	v_rndne_f32_e32 v11, v11
	v_max_f32_e32 v11, 1.0, v11
	v_cvt_pk_u8_f32 v7, v11, 2, v7
	v_mul_f32_e32 v11, 0x437f0000, v14
	v_rndne_f32_e32 v11, v11
	v_max_f32_e32 v11, 1.0, v11
	v_cvt_pk_u8_f32 v11, v11, 3, v7
	v_lshl_add_u64 v[12:13], v[12:13], 0, v[2:3]
	v_mul_f32_e32 v7, 0xbfb8aa3b, v62
	global_store_dwordx4 v[12:13], v[8:11], off
	v_exp_f32_e32 v7, v7
	v_mul_f32_e32 v14, 0xbfb8aa3b, v52
	v_add_u32_e32 v8, 0xa0, v6
	v_mad_i64_i32 v[12:13], s[54:55], v8, s12, v[4:5]
	v_mul_f32_e32 v8, 0xbfb8aa3b, v63
	v_exp_f32_e32 v8, v8
	v_add_f32_e32 v7, 1.0, v7
	v_rcp_f32_e32 v7, v7
	v_mul_f32_e32 v9, 0xbfb8aa3b, v64
	v_add_f32_e32 v8, 1.0, v8
	v_rcp_f32_e32 v8, v8
	v_mul_f32_e32 v7, 0x437f0000, v7
	v_rndne_f32_e32 v7, v7
	v_max_f32_e32 v7, 1.0, v7
	v_mul_f32_e32 v8, 0x437f0000, v8
	v_rndne_f32_e32 v8, v8
	v_cvt_pk_u8_f32 v7, v7, 0, 0
	v_max_f32_e32 v8, 1.0, v8
	v_exp_f32_e32 v9, v9
	v_cvt_pk_u8_f32 v7, v8, 1, v7
	v_mul_f32_e32 v8, 0xbfb8aa3b, v65
	v_exp_f32_e32 v8, v8
	v_add_f32_e32 v9, 1.0, v9
	v_rcp_f32_e32 v9, v9
	v_mul_f32_e32 v10, 0xbfb8aa3b, v60
	v_add_f32_e32 v8, 1.0, v8
	v_rcp_f32_e32 v8, v8
	v_mul_f32_e32 v9, 0x437f0000, v9
	v_rndne_f32_e32 v9, v9
	v_max_f32_e32 v9, 1.0, v9
	v_mul_f32_e32 v8, 0x437f0000, v8
	v_rndne_f32_e32 v8, v8
	v_cvt_pk_u8_f32 v7, v9, 2, v7
	v_mul_f32_e32 v9, 0xbfb8aa3b, v58
	v_max_f32_e32 v8, 1.0, v8
	v_exp_f32_e32 v9, v9
	v_cvt_pk_u8_f32 v8, v8, 3, v7
	v_mul_f32_e32 v7, 0xbfb8aa3b, v59
	v_exp_f32_e32 v7, v7
	v_add_f32_e32 v9, 1.0, v9
	v_rcp_f32_e32 v9, v9
	v_exp_f32_e32 v10, v10
	v_add_f32_e32 v7, 1.0, v7
	v_rcp_f32_e32 v7, v7
	v_mul_f32_e32 v9, 0x437f0000, v9
	v_rndne_f32_e32 v9, v9
	v_max_f32_e32 v9, 1.0, v9
	v_mul_f32_e32 v7, 0x437f0000, v7
	v_rndne_f32_e32 v7, v7
	v_cvt_pk_u8_f32 v9, v9, 0, 0
	v_max_f32_e32 v7, 1.0, v7
	v_cvt_pk_u8_f32 v7, v7, 1, v9
	v_mul_f32_e32 v9, 0xbfb8aa3b, v61
	v_exp_f32_e32 v9, v9
	v_add_f32_e32 v10, 1.0, v10
	v_rcp_f32_e32 v10, v10
	v_mul_f32_e32 v11, 0xbfb8aa3b, v56
	v_add_f32_e32 v9, 1.0, v9
	v_rcp_f32_e32 v9, v9
	v_mul_f32_e32 v10, 0x437f0000, v10
	v_rndne_f32_e32 v10, v10
	v_max_f32_e32 v10, 1.0, v10
	v_mul_f32_e32 v9, 0x437f0000, v9
	v_rndne_f32_e32 v9, v9
	v_cvt_pk_u8_f32 v7, v10, 2, v7
	v_mul_f32_e32 v10, 0xbfb8aa3b, v54
	v_max_f32_e32 v9, 1.0, v9
	v_exp_f32_e32 v10, v10
	v_cvt_pk_u8_f32 v9, v9, 3, v7
	v_mul_f32_e32 v7, 0xbfb8aa3b, v55
	v_exp_f32_e32 v7, v7
	v_add_f32_e32 v10, 1.0, v10
	v_rcp_f32_e32 v10, v10
	v_exp_f32_e32 v11, v11
	v_add_f32_e32 v7, 1.0, v7
	v_rcp_f32_e32 v7, v7
	v_mul_f32_e32 v10, 0x437f0000, v10
	v_rndne_f32_e32 v10, v10
	v_max_f32_e32 v10, 1.0, v10
	v_mul_f32_e32 v7, 0x437f0000, v7
	v_rndne_f32_e32 v7, v7
	v_cvt_pk_u8_f32 v10, v10, 0, 0
	v_max_f32_e32 v7, 1.0, v7
	v_cvt_pk_u8_f32 v7, v7, 1, v10
	v_mul_f32_e32 v10, 0xbfb8aa3b, v57
	v_exp_f32_e32 v10, v10
	v_add_f32_e32 v11, 1.0, v11
	v_rcp_f32_e32 v11, v11
	v_exp_f32_e32 v14, v14
	v_add_f32_e32 v10, 1.0, v10
	v_rcp_f32_e32 v10, v10
	v_mul_f32_e32 v11, 0x437f0000, v11
	v_rndne_f32_e32 v11, v11
	v_max_f32_e32 v11, 1.0, v11
	v_mul_f32_e32 v10, 0x437f0000, v10
	v_rndne_f32_e32 v10, v10
	v_cvt_pk_u8_f32 v7, v11, 2, v7
	v_mul_f32_e32 v11, 0xbfb8aa3b, v50
	v_max_f32_e32 v10, 1.0, v10
	v_exp_f32_e32 v11, v11
	v_cvt_pk_u8_f32 v10, v10, 3, v7
	v_mul_f32_e32 v7, 0xbfb8aa3b, v51
	v_exp_f32_e32 v7, v7
	v_add_f32_e32 v11, 1.0, v11
	v_rcp_f32_e32 v11, v11
	v_add_f32_e32 v14, 1.0, v14
	v_add_f32_e32 v7, 1.0, v7
	v_rcp_f32_e32 v7, v7
	v_mul_f32_e32 v15, 0xbfb8aa3b, v53
	v_mul_f32_e32 v11, 0x437f0000, v11
	v_rcp_f32_e32 v14, v14
	v_exp_f32_e32 v15, v15
	v_rndne_f32_e32 v11, v11
	v_mul_f32_e32 v7, 0x437f0000, v7
	v_max_f32_e32 v11, 1.0, v11
	v_rndne_f32_e32 v7, v7
	v_cvt_pk_u8_f32 v11, v11, 0, 0
	v_max_f32_e32 v7, 1.0, v7
	v_cvt_pk_u8_f32 v7, v7, 1, v11
	v_mul_f32_e32 v11, 0x437f0000, v14
	v_add_f32_e32 v14, 1.0, v15
	v_rcp_f32_e32 v14, v14
	v_rndne_f32_e32 v11, v11
	v_max_f32_e32 v11, 1.0, v11
	v_cvt_pk_u8_f32 v7, v11, 2, v7
	v_mul_f32_e32 v11, 0x437f0000, v14
	v_rndne_f32_e32 v11, v11
	v_max_f32_e32 v11, 1.0, v11
	v_cvt_pk_u8_f32 v11, v11, 3, v7
	v_mul_f32_e32 v7, 0xbfb8aa3b, v46
	v_lshl_add_u64 v[12:13], v[12:13], 0, v[2:3]
	v_add_u32_e32 v6, 0xb0, v6
	v_exp_f32_e32 v7, v7
	global_store_dwordx4 v[12:13], v[8:11], off
	v_mul_f32_e32 v12, 0xbfb8aa3b, v37
	v_exp_f32_e32 v12, v12
	v_mad_i64_i32 v[8:9], s[54:55], v6, s12, v[4:5]
	v_mul_f32_e32 v4, 0xbfb8aa3b, v47
	v_exp_f32_e32 v4, v4
	v_add_f32_e32 v7, 1.0, v7
	v_rcp_f32_e32 v7, v7
	v_mul_f32_e32 v6, 0xbfb8aa3b, v48
	v_add_f32_e32 v4, 1.0, v4
	v_rcp_f32_e32 v4, v4
	v_mul_f32_e32 v5, 0x437f0000, v7
	v_rndne_f32_e32 v5, v5
	v_max_f32_e32 v5, 1.0, v5
	v_mul_f32_e32 v4, 0x437f0000, v4
	v_rndne_f32_e32 v4, v4
	v_cvt_pk_u8_f32 v5, v5, 0, 0
	v_max_f32_e32 v4, 1.0, v4
	v_exp_f32_e32 v6, v6
	v_cvt_pk_u8_f32 v4, v4, 1, v5
	v_mul_f32_e32 v5, 0xbfb8aa3b, v49
	v_exp_f32_e32 v5, v5
	v_add_f32_e32 v6, 1.0, v6
	v_rcp_f32_e32 v6, v6
	v_mul_f32_e32 v7, 0xbfb8aa3b, v44
	v_add_f32_e32 v5, 1.0, v5
	v_rcp_f32_e32 v5, v5
	v_mul_f32_e32 v6, 0x437f0000, v6
	v_rndne_f32_e32 v6, v6
	v_max_f32_e32 v6, 1.0, v6
	v_mul_f32_e32 v5, 0x437f0000, v5
	v_rndne_f32_e32 v5, v5
	v_cvt_pk_u8_f32 v4, v6, 2, v4
	v_mul_f32_e32 v6, 0xbfb8aa3b, v42
	v_max_f32_e32 v5, 1.0, v5
	v_exp_f32_e32 v6, v6
	v_cvt_pk_u8_f32 v4, v5, 3, v4
	v_mul_f32_e32 v5, 0xbfb8aa3b, v43
	v_exp_f32_e32 v5, v5
	v_add_f32_e32 v6, 1.0, v6
	v_rcp_f32_e32 v6, v6
	v_exp_f32_e32 v7, v7
	v_add_f32_e32 v5, 1.0, v5
	v_rcp_f32_e32 v5, v5
	v_mul_f32_e32 v6, 0x437f0000, v6
	v_rndne_f32_e32 v6, v6
	v_max_f32_e32 v6, 1.0, v6
	v_mul_f32_e32 v5, 0x437f0000, v5
	v_rndne_f32_e32 v5, v5
	v_cvt_pk_u8_f32 v6, v6, 0, 0
	v_max_f32_e32 v5, 1.0, v5
	v_cvt_pk_u8_f32 v5, v5, 1, v6
	v_mul_f32_e32 v6, 0xbfb8aa3b, v45
	v_exp_f32_e32 v6, v6
	v_add_f32_e32 v7, 1.0, v7
	v_rcp_f32_e32 v7, v7
	v_mul_f32_e32 v10, 0xbfb8aa3b, v40
	v_add_f32_e32 v6, 1.0, v6
	v_rcp_f32_e32 v6, v6
	v_mul_f32_e32 v7, 0x437f0000, v7
	v_rndne_f32_e32 v7, v7
	v_max_f32_e32 v7, 1.0, v7
	v_mul_f32_e32 v6, 0x437f0000, v6
	v_rndne_f32_e32 v6, v6
	v_cvt_pk_u8_f32 v5, v7, 2, v5
	v_mul_f32_e32 v7, 0xbfb8aa3b, v38
	v_max_f32_e32 v6, 1.0, v6
	v_exp_f32_e32 v7, v7
	v_cvt_pk_u8_f32 v5, v6, 3, v5
	v_mul_f32_e32 v6, 0xbfb8aa3b, v39
	v_exp_f32_e32 v6, v6
	v_add_f32_e32 v7, 1.0, v7
	v_rcp_f32_e32 v7, v7
	v_exp_f32_e32 v10, v10
	v_add_f32_e32 v6, 1.0, v6
	v_rcp_f32_e32 v6, v6
	v_mul_f32_e32 v7, 0x437f0000, v7
	v_rndne_f32_e32 v7, v7
	v_max_f32_e32 v7, 1.0, v7
	v_mul_f32_e32 v6, 0x437f0000, v6
	v_rndne_f32_e32 v6, v6
	v_cvt_pk_u8_f32 v7, v7, 0, 0
	v_max_f32_e32 v6, 1.0, v6
	v_cvt_pk_u8_f32 v6, v6, 1, v7
	v_mul_f32_e32 v7, 0xbfb8aa3b, v41
	v_exp_f32_e32 v7, v7
	v_add_f32_e32 v10, 1.0, v10
	v_rcp_f32_e32 v10, v10
	v_mul_f32_e32 v11, 0xbfb8aa3b, v36
	v_add_f32_e32 v7, 1.0, v7
	v_rcp_f32_e32 v7, v7
	v_mul_f32_e32 v10, 0x437f0000, v10
	v_rndne_f32_e32 v10, v10
	v_max_f32_e32 v10, 1.0, v10
	v_mul_f32_e32 v7, 0x437f0000, v7
	v_rndne_f32_e32 v7, v7
	v_cvt_pk_u8_f32 v6, v10, 2, v6
	v_mul_f32_e32 v10, 0xbfb8aa3b, v34
	v_max_f32_e32 v7, 1.0, v7
	v_exp_f32_e32 v10, v10
	v_cvt_pk_u8_f32 v6, v7, 3, v6
	v_mul_f32_e32 v7, 0xbfb8aa3b, v35
	v_exp_f32_e32 v7, v7
	v_add_f32_e32 v10, 1.0, v10
	v_exp_f32_e32 v11, v11
	v_rcp_f32_e32 v10, v10
	v_add_f32_e32 v7, 1.0, v7
	v_rcp_f32_e32 v7, v7
	v_add_f32_e32 v11, 1.0, v11
	v_mul_f32_e32 v10, 0x437f0000, v10
	v_rcp_f32_e32 v11, v11
	v_rndne_f32_e32 v10, v10
	v_mul_f32_e32 v7, 0x437f0000, v7
	v_max_f32_e32 v10, 1.0, v10
	v_rndne_f32_e32 v7, v7
	v_cvt_pk_u8_f32 v10, v10, 0, 0
	v_max_f32_e32 v7, 1.0, v7
	v_cvt_pk_u8_f32 v7, v7, 1, v10
	v_mul_f32_e32 v10, 0x437f0000, v11
	v_add_f32_e32 v11, 1.0, v12
	v_rcp_f32_e32 v11, v11
	v_rndne_f32_e32 v10, v10
	v_max_f32_e32 v10, 1.0, v10
	v_cvt_pk_u8_f32 v7, v10, 2, v7
	v_mul_f32_e32 v10, 0x437f0000, v11
	v_rndne_f32_e32 v10, v10
	v_max_f32_e32 v10, 1.0, v10
	v_cvt_pk_u8_f32 v7, v10, 3, v7
	v_lshl_add_u64 v[2:3], v[8:9], 0, v[2:3]
	s_and_b64 vcc, exec, s[38:39]
	s_mov_b64 s[38:39], -1
	global_store_dwordx4 v[2:3], v[4:7], off
	s_cbranch_vccnz .LBB0_136
	s_andn2_b64 vcc, exec, s[44:45]
	s_cbranch_vccnz .LBB0_135
	s_barrier
	s_branch .LBB0_135

.LBB0_738:
	v_mov_b32_e32 v0, v165
	s_add_i32 s87, s87, s77
	v_readlane_b32 s100, v252, 5
	s_cmp_ge_u32 s100, 4
	s_cbranch_scc0 .Lepi_prio_2
	s_setprio 1
.Lepi_prio_2:
	s_nop 15
	s_nop 15
	s_movk_i32 s12, 0x1800
	v_and_or_b32 v2, v0, 15, s87
	v_mul_lo_u32 v3, v2, s12
	v_and_b32_e32 v0, -16, v0
	s_add_i32 s12, s82, s86
	v_add3_u32 v6, s12, v0, v3
	v_lshlrev_b32_e32 v2, 11, v2
	s_or_b32 s12, s86, s81
	v_add3_u32 v0, s12, v0, v2
	global_load_dwordx4 v[152:155], v6, s[46:47]
	v_add_u32_e32 v204, 0x18000, v6
	global_load_dwordx4 v[156:159], v204, s[46:47]
	v_add_u32_e32 v204, 0x30000, v6
	global_load_dwordx4 v[160:163], v204, s[46:47]
	v_add_u32_e32 v204, 0x48000, v6
	global_load_dwordx4 v[172:175], v204, s[46:47]
	v_add_u32_e32 v204, 0xc0000, v6
	global_load_dwordx4 v[176:179], v204, s[46:47]
	v_add_u32_e32 v204, 0xd8000, v6
	global_load_dwordx4 v[180:183], v204, s[46:47]
	v_add_u32_e32 v204, 0xf0000, v6
	global_load_dwordx4 v[184:187], v204, s[46:47]
	v_add_u32_e32 v204, 0x108000, v6
	global_load_dwordx4 v[188:191], v204, s[46:47]
	s_mov_b64 s[56:57], -1
	s_and_b64 vcc, exec, s[38:39]
	s_movk_i32 s89, 0xfe3f
	s_waitcnt vmcnt(7)
	v_cvt_f32_ubyte0_e32 v7, v152
	v_cvt_f32_ubyte1_e32 v8, v152
	v_mul_f32_e32 v7, 0x3b808081, v7
	v_mul_f32_e32 v8, 0x3b808081, v8
	v_cvt_f32_ubyte2_e32 v9, v152
	v_cvt_f32_ubyte3_e32 v2, v152
	v_mul_f32_e32 v7, v142, v7
	v_mul_f32_e32 v8, v143, v8
	v_mul_f32_e32 v2, 0x3b808081, v2
	v_mul_f32_e32 v10, v145, v2
	v_med3_f32 v7, v7, s19, v229
	v_med3_f32 v8, v8, s19, v229
	v_mov_b32_e32 v2, v1
	v_cvt_pk_fp8_f32 v2, v7, v8
	v_mul_f32_e32 v9, 0x3b808081, v9
	v_mul_f32_e32 v9, v144, v9
	v_med3_f32 v7, v9, s19, v229
	v_med3_f32 v8, v10, s19, v229
	v_cvt_pk_fp8_f32 v2, v7, v8 op_sel:[0,0,1]
	v_cvt_f32_ubyte0_e32 v7, v153
	v_cvt_f32_ubyte1_e32 v8, v153
	v_mul_f32_e32 v7, 0x3b808081, v7
	v_mul_f32_e32 v8, 0x3b808081, v8
	v_cvt_f32_ubyte2_e32 v9, v153
	v_cvt_f32_ubyte3_e32 v3, v153
	v_mul_f32_e32 v7, v138, v7
	v_mul_f32_e32 v8, v139, v8
	v_mul_f32_e32 v3, 0x3b808081, v3
	v_mul_f32_e32 v10, v141, v3
	v_med3_f32 v7, v7, s19, v229
	v_med3_f32 v8, v8, s19, v229
	v_mov_b32_e32 v3, v1
	v_cvt_pk_fp8_f32 v3, v7, v8
	v_mul_f32_e32 v9, 0x3b808081, v9
	v_mul_f32_e32 v9, v140, v9
	v_med3_f32 v7, v9, s19, v229
	v_med3_f32 v8, v10, s19, v229
	v_cvt_pk_fp8_f32 v3, v7, v8 op_sel:[0,0,1]
	v_cvt_f32_ubyte0_e32 v7, v154
	v_cvt_f32_ubyte1_e32 v8, v154
	v_mul_f32_e32 v7, 0x3b808081, v7
	v_mul_f32_e32 v8, 0x3b808081, v8
	v_cvt_f32_ubyte2_e32 v9, v154
	v_cvt_f32_ubyte3_e32 v4, v154
	v_mul_f32_e32 v7, v134, v7
	v_mul_f32_e32 v8, v135, v8
	v_mul_f32_e32 v4, 0x3b808081, v4
	v_mul_f32_e32 v10, v137, v4
	v_med3_f32 v7, v7, s19, v229
	v_med3_f32 v8, v8, s19, v229
	v_mov_b32_e32 v4, v1
	v_cvt_pk_fp8_f32 v4, v7, v8
	v_mul_f32_e32 v9, 0x3b808081, v9
	v_mul_f32_e32 v9, v136, v9
	v_med3_f32 v7, v9, s19, v229
	v_med3_f32 v8, v10, s19, v229
	v_cvt_pk_fp8_f32 v4, v7, v8 op_sel:[0,0,1]
	v_cvt_f32_ubyte0_e32 v7, v155
	v_cvt_f32_ubyte1_e32 v8, v155
	v_mul_f32_e32 v7, 0x3b808081, v7
	v_mul_f32_e32 v8, 0x3b808081, v8
	v_cvt_f32_ubyte2_e32 v9, v155
	v_cvt_f32_ubyte3_e32 v5, v155
	v_mul_f32_e32 v7, v130, v7
	v_mul_f32_e32 v8, v131, v8
	v_mul_f32_e32 v5, 0x3b808081, v5
	v_mul_f32_e32 v10, v133, v5
	v_med3_f32 v7, v7, s19, v229
	v_med3_f32 v8, v8, s19, v229
	v_mov_b32_e32 v5, v1
	v_cvt_pk_fp8_f32 v5, v7, v8
	v_mul_f32_e32 v9, 0x3b808081, v9
	v_mul_f32_e32 v9, v132, v9
	v_med3_f32 v7, v9, s19, v229
	v_med3_f32 v8, v10, s19, v229
	v_cvt_pk_fp8_f32 v5, v7, v8 op_sel:[0,0,1]
	global_store_dwordx4 v0, v[2:5], s[48:49]
	s_nop 1
	s_waitcnt vmcnt(7)
	v_cvt_f32_ubyte0_e32 v7, v156
	v_cvt_f32_ubyte1_e32 v8, v156
	v_mul_f32_e32 v7, 0x3b808081, v7
	v_mul_f32_e32 v8, 0x3b808081, v8
	v_cvt_f32_ubyte2_e32 v9, v156
	v_cvt_f32_ubyte3_e32 v2, v156
	v_mul_f32_e32 v7, v126, v7
	v_mul_f32_e32 v8, v127, v8
	v_mul_f32_e32 v2, 0x3b808081, v2
	v_mul_f32_e32 v10, v129, v2
	v_med3_f32 v7, v7, s19, v229
	v_med3_f32 v8, v8, s19, v229
	v_mov_b32_e32 v2, v1
	v_cvt_pk_fp8_f32 v2, v7, v8
	v_mul_f32_e32 v9, 0x3b808081, v9
	v_mul_f32_e32 v9, v128, v9
	v_med3_f32 v7, v9, s19, v229
	v_med3_f32 v8, v10, s19, v229
	v_cvt_pk_fp8_f32 v2, v7, v8 op_sel:[0,0,1]
	v_cvt_f32_ubyte0_e32 v7, v157
	v_cvt_f32_ubyte1_e32 v8, v157
	v_mul_f32_e32 v7, 0x3b808081, v7
	v_mul_f32_e32 v8, 0x3b808081, v8
	v_cvt_f32_ubyte2_e32 v9, v157
	v_cvt_f32_ubyte3_e32 v3, v157
	v_mul_f32_e32 v7, v122, v7
	v_mul_f32_e32 v8, v123, v8
	v_mul_f32_e32 v3, 0x3b808081, v3
	v_mul_f32_e32 v10, v125, v3
	v_med3_f32 v7, v7, s19, v229
	v_med3_f32 v8, v8, s19, v229
	v_mov_b32_e32 v3, v1
	v_cvt_pk_fp8_f32 v3, v7, v8
	v_mul_f32_e32 v9, 0x3b808081, v9
	v_mul_f32_e32 v9, v124, v9
	v_med3_f32 v7, v9, s19, v229
	v_med3_f32 v8, v10, s19, v229
	v_cvt_pk_fp8_f32 v3, v7, v8 op_sel:[0,0,1]
	v_cvt_f32_ubyte0_e32 v7, v158
	v_cvt_f32_ubyte1_e32 v8, v158
	v_mul_f32_e32 v7, 0x3b808081, v7
	v_mul_f32_e32 v8, 0x3b808081, v8
	v_cvt_f32_ubyte2_e32 v9, v158
	v_cvt_f32_ubyte3_e32 v4, v158
	v_mul_f32_e32 v7, v118, v7
	v_mul_f32_e32 v8, v119, v8
	v_mul_f32_e32 v4, 0x3b808081, v4
	v_mul_f32_e32 v10, v121, v4
	v_med3_f32 v7, v7, s19, v229
	v_med3_f32 v8, v8, s19, v229
	v_mov_b32_e32 v4, v1
	v_cvt_pk_fp8_f32 v4, v7, v8
	v_mul_f32_e32 v9, 0x3b808081, v9
	v_mul_f32_e32 v9, v120, v9
	v_med3_f32 v7, v9, s19, v229
	v_med3_f32 v8, v10, s19, v229
	v_cvt_pk_fp8_f32 v4, v7, v8 op_sel:[0,0,1]
	v_cvt_f32_ubyte0_e32 v7, v159
	v_cvt_f32_ubyte1_e32 v8, v159
	v_mul_f32_e32 v7, 0x3b808081, v7
	v_mul_f32_e32 v8, 0x3b808081, v8
	v_cvt_f32_ubyte2_e32 v9, v159
	v_cvt_f32_ubyte3_e32 v5, v159
	v_mul_f32_e32 v7, v114, v7
	v_mul_f32_e32 v8, v115, v8
	v_mul_f32_e32 v5, 0x3b808081, v5
	v_mul_f32_e32 v10, v117, v5
	v_med3_f32 v7, v7, s19, v229
	v_med3_f32 v8, v8, s19, v229
	v_mov_b32_e32 v5, v1
	v_cvt_pk_fp8_f32 v5, v7, v8
	v_mul_f32_e32 v9, 0x3b808081, v9
	v_mul_f32_e32 v9, v116, v9
	v_med3_f32 v7, v9, s19, v229
	v_med3_f32 v8, v10, s19, v229
	v_cvt_pk_fp8_f32 v5, v7, v8 op_sel:[0,0,1]
	v_add_u32_e32 v7, 0x8000, v0
	global_store_dwordx4 v7, v[2:5], s[48:49]
	s_nop 1
	s_waitcnt vmcnt(7)
	v_cvt_f32_ubyte0_e32 v7, v160
	v_cvt_f32_ubyte1_e32 v8, v160
	v_mul_f32_e32 v7, 0x3b808081, v7
	v_mul_f32_e32 v8, 0x3b808081, v8
	v_cvt_f32_ubyte2_e32 v9, v160
	v_cvt_f32_ubyte3_e32 v2, v160
	v_mul_f32_e32 v7, v110, v7
	v_mul_f32_e32 v8, v111, v8
	v_mul_f32_e32 v2, 0x3b808081, v2
	v_mul_f32_e32 v10, v113, v2
	v_med3_f32 v7, v7, s19, v229
	v_med3_f32 v8, v8, s19, v229
	v_mov_b32_e32 v2, v1
	v_cvt_pk_fp8_f32 v2, v7, v8
	v_mul_f32_e32 v9, 0x3b808081, v9
	v_mul_f32_e32 v9, v112, v9
	v_med3_f32 v7, v9, s19, v229
	v_med3_f32 v8, v10, s19, v229
	v_cvt_pk_fp8_f32 v2, v7, v8 op_sel:[0,0,1]
	v_cvt_f32_ubyte0_e32 v7, v161
	v_cvt_f32_ubyte1_e32 v8, v161
	v_mul_f32_e32 v7, 0x3b808081, v7
	v_mul_f32_e32 v8, 0x3b808081, v8
	v_cvt_f32_ubyte2_e32 v9, v161
	v_cvt_f32_ubyte3_e32 v3, v161
	v_mul_f32_e32 v7, v106, v7
	v_mul_f32_e32 v8, v107, v8
	v_mul_f32_e32 v3, 0x3b808081, v3
	v_mul_f32_e32 v10, v109, v3
	v_med3_f32 v7, v7, s19, v229
	v_med3_f32 v8, v8, s19, v229
	v_mov_b32_e32 v3, v1
	v_cvt_pk_fp8_f32 v3, v7, v8
	v_mul_f32_e32 v9, 0x3b808081, v9
	v_mul_f32_e32 v9, v108, v9
	v_med3_f32 v7, v9, s19, v229
	v_med3_f32 v8, v10, s19, v229
	v_cvt_pk_fp8_f32 v3, v7, v8 op_sel:[0,0,1]
	v_cvt_f32_ubyte0_e32 v7, v162
	v_cvt_f32_ubyte1_e32 v8, v162
	v_mul_f32_e32 v7, 0x3b808081, v7
	v_mul_f32_e32 v8, 0x3b808081, v8
	v_cvt_f32_ubyte2_e32 v9, v162
	v_cvt_f32_ubyte3_e32 v4, v162
	v_mul_f32_e32 v7, v102, v7
	v_mul_f32_e32 v8, v103, v8
	v_mul_f32_e32 v4, 0x3b808081, v4
	v_mul_f32_e32 v10, v105, v4
	v_med3_f32 v7, v7, s19, v229
	v_med3_f32 v8, v8, s19, v229
	v_mov_b32_e32 v4, v1
	v_cvt_pk_fp8_f32 v4, v7, v8
	v_mul_f32_e32 v9, 0x3b808081, v9
	v_mul_f32_e32 v9, v104, v9
	v_med3_f32 v7, v9, s19, v229
	v_med3_f32 v8, v10, s19, v229
	v_cvt_pk_fp8_f32 v4, v7, v8 op_sel:[0,0,1]
	v_cvt_f32_ubyte0_e32 v7, v163
	v_cvt_f32_ubyte1_e32 v8, v163
	v_mul_f32_e32 v7, 0x3b808081, v7
	v_mul_f32_e32 v8, 0x3b808081, v8
	v_cvt_f32_ubyte2_e32 v9, v163
	v_cvt_f32_ubyte3_e32 v5, v163
	v_mul_f32_e32 v7, v98, v7
	v_mul_f32_e32 v8, v99, v8
	v_mul_f32_e32 v5, 0x3b808081, v5
	v_mul_f32_e32 v10, v101, v5
	v_med3_f32 v7, v7, s19, v229
	v_med3_f32 v8, v8, s19, v229
	v_mov_b32_e32 v5, v1
	v_cvt_pk_fp8_f32 v5, v7, v8
	v_mul_f32_e32 v9, 0x3b808081, v9
	v_mul_f32_e32 v9, v100, v9
	v_med3_f32 v7, v9, s19, v229
	v_med3_f32 v8, v10, s19, v229
	v_cvt_pk_fp8_f32 v5, v7, v8 op_sel:[0,0,1]
	v_add_u32_e32 v7, 0x10000, v0
	global_store_dwordx4 v7, v[2:5], s[48:49]
	s_nop 1
	s_waitcnt vmcnt(7)
	v_cvt_f32_ubyte0_e32 v7, v172
	v_cvt_f32_ubyte1_e32 v8, v172
	v_mul_f32_e32 v7, 0x3b808081, v7
	v_mul_f32_e32 v8, 0x3b808081, v8
	v_cvt_f32_ubyte2_e32 v9, v172
	v_cvt_f32_ubyte3_e32 v2, v172
	v_mul_f32_e32 v7, v94, v7
	v_mul_f32_e32 v8, v95, v8
	v_mul_f32_e32 v2, 0x3b808081, v2
	v_mul_f32_e32 v10, v97, v2
	v_med3_f32 v7, v7, s19, v229
	v_med3_f32 v8, v8, s19, v229
	v_mov_b32_e32 v2, v1
	v_cvt_pk_fp8_f32 v2, v7, v8
	v_mul_f32_e32 v9, 0x3b808081, v9
	v_mul_f32_e32 v9, v96, v9
	v_med3_f32 v7, v9, s19, v229
	v_med3_f32 v8, v10, s19, v229
	v_cvt_pk_fp8_f32 v2, v7, v8 op_sel:[0,0,1]
	v_cvt_f32_ubyte0_e32 v7, v173
	v_cvt_f32_ubyte1_e32 v8, v173
	v_mul_f32_e32 v7, 0x3b808081, v7
	v_mul_f32_e32 v8, 0x3b808081, v8
	v_cvt_f32_ubyte2_e32 v9, v173
	v_cvt_f32_ubyte3_e32 v3, v173
	v_mul_f32_e32 v7, v90, v7
	v_mul_f32_e32 v8, v91, v8
	v_mul_f32_e32 v3, 0x3b808081, v3
	v_mul_f32_e32 v10, v93, v3
	v_med3_f32 v7, v7, s19, v229
	v_med3_f32 v8, v8, s19, v229
	v_mov_b32_e32 v3, v1
	v_cvt_pk_fp8_f32 v3, v7, v8
	v_mul_f32_e32 v9, 0x3b808081, v9
	v_mul_f32_e32 v9, v92, v9
	v_med3_f32 v7, v9, s19, v229
	v_med3_f32 v8, v10, s19, v229
	v_cvt_pk_fp8_f32 v3, v7, v8 op_sel:[0,0,1]
	v_cvt_f32_ubyte0_e32 v7, v174
	v_cvt_f32_ubyte1_e32 v8, v174
	v_mul_f32_e32 v7, 0x3b808081, v7
	v_mul_f32_e32 v8, 0x3b808081, v8
	v_cvt_f32_ubyte2_e32 v9, v174
	v_cvt_f32_ubyte3_e32 v4, v174
	v_mul_f32_e32 v7, v86, v7
	v_mul_f32_e32 v8, v87, v8
	v_mul_f32_e32 v4, 0x3b808081, v4
	v_mul_f32_e32 v10, v89, v4
	v_med3_f32 v7, v7, s19, v229
	v_med3_f32 v8, v8, s19, v229
	v_mov_b32_e32 v4, v1
	v_cvt_pk_fp8_f32 v4, v7, v8
	v_mul_f32_e32 v9, 0x3b808081, v9
	v_mul_f32_e32 v9, v88, v9
	v_med3_f32 v7, v9, s19, v229
	v_med3_f32 v8, v10, s19, v229
	v_cvt_pk_fp8_f32 v4, v7, v8 op_sel:[0,0,1]
	v_cvt_f32_ubyte0_e32 v7, v175
	v_cvt_f32_ubyte1_e32 v8, v175
	v_mul_f32_e32 v7, 0x3b808081, v7
	v_mul_f32_e32 v8, 0x3b808081, v8
	v_cvt_f32_ubyte2_e32 v9, v175
	v_cvt_f32_ubyte3_e32 v5, v175
	v_mul_f32_e32 v7, v82, v7
	v_mul_f32_e32 v8, v83, v8
	v_mul_f32_e32 v5, 0x3b808081, v5
	v_mul_f32_e32 v10, v85, v5
	v_med3_f32 v7, v7, s19, v229
	v_med3_f32 v8, v8, s19, v229
	v_mov_b32_e32 v5, v1
	v_cvt_pk_fp8_f32 v5, v7, v8
	v_mul_f32_e32 v9, 0x3b808081, v9
	v_mul_f32_e32 v9, v84, v9
	v_med3_f32 v7, v9, s19, v229
	v_med3_f32 v8, v10, s19, v229
	v_cvt_pk_fp8_f32 v5, v7, v8 op_sel:[0,0,1]
	v_add_u32_e32 v7, 0x18000, v0
	global_store_dwordx4 v7, v[2:5], s[48:49]
	s_nop 1
	s_waitcnt vmcnt(7)
	v_cvt_f32_ubyte0_e32 v7, v176
	v_cvt_f32_ubyte1_e32 v8, v176
	v_mul_f32_e32 v7, 0x3b808081, v7
	v_mul_f32_e32 v8, 0x3b808081, v8
	v_cvt_f32_ubyte2_e32 v9, v176
	v_cvt_f32_ubyte3_e32 v2, v176
	v_mul_f32_e32 v7, v78, v7
	v_mul_f32_e32 v8, v79, v8
	v_mul_f32_e32 v2, 0x3b808081, v2
	v_mul_f32_e32 v10, v81, v2
	v_med3_f32 v7, v7, s19, v229
	v_med3_f32 v8, v8, s19, v229
	v_mov_b32_e32 v2, v1
	v_cvt_pk_fp8_f32 v2, v7, v8
	v_mul_f32_e32 v9, 0x3b808081, v9
	v_mul_f32_e32 v9, v80, v9
	v_med3_f32 v7, v9, s19, v229
	v_med3_f32 v8, v10, s19, v229
	v_cvt_pk_fp8_f32 v2, v7, v8 op_sel:[0,0,1]
	v_cvt_f32_ubyte0_e32 v7, v177
	v_cvt_f32_ubyte1_e32 v8, v177
	v_mul_f32_e32 v7, 0x3b808081, v7
	v_mul_f32_e32 v8, 0x3b808081, v8
	v_cvt_f32_ubyte2_e32 v9, v177
	v_cvt_f32_ubyte3_e32 v3, v177
	v_mul_f32_e32 v7, v74, v7
	v_mul_f32_e32 v8, v75, v8
	v_mul_f32_e32 v3, 0x3b808081, v3
	v_mul_f32_e32 v10, v77, v3
	v_med3_f32 v7, v7, s19, v229
	v_med3_f32 v8, v8, s19, v229
	v_mov_b32_e32 v3, v1
	v_cvt_pk_fp8_f32 v3, v7, v8
	v_mul_f32_e32 v9, 0x3b808081, v9
	v_mul_f32_e32 v9, v76, v9
	v_med3_f32 v7, v9, s19, v229
	v_med3_f32 v8, v10, s19, v229
	v_cvt_pk_fp8_f32 v3, v7, v8 op_sel:[0,0,1]
	v_cvt_f32_ubyte0_e32 v7, v178
	v_cvt_f32_ubyte1_e32 v8, v178
	v_mul_f32_e32 v7, 0x3b808081, v7
	v_mul_f32_e32 v8, 0x3b808081, v8
	v_cvt_f32_ubyte2_e32 v9, v178
	v_cvt_f32_ubyte3_e32 v4, v178
	v_mul_f32_e32 v7, v70, v7
	v_mul_f32_e32 v8, v71, v8
	v_mul_f32_e32 v4, 0x3b808081, v4
	v_mul_f32_e32 v10, v73, v4
	v_med3_f32 v7, v7, s19, v229
	v_med3_f32 v8, v8, s19, v229
	v_mov_b32_e32 v4, v1
	v_cvt_pk_fp8_f32 v4, v7, v8
	v_mul_f32_e32 v9, 0x3b808081, v9
	v_mul_f32_e32 v9, v72, v9
	v_med3_f32 v7, v9, s19, v229
	v_med3_f32 v8, v10, s19, v229
	v_cvt_pk_fp8_f32 v4, v7, v8 op_sel:[0,0,1]
	v_cvt_f32_ubyte0_e32 v7, v179
	v_cvt_f32_ubyte1_e32 v8, v179
	v_mul_f32_e32 v7, 0x3b808081, v7
	v_mul_f32_e32 v8, 0x3b808081, v8
	v_cvt_f32_ubyte2_e32 v9, v179
	v_cvt_f32_ubyte3_e32 v5, v179
	v_mul_f32_e32 v7, v66, v7
	v_mul_f32_e32 v8, v67, v8
	v_mul_f32_e32 v5, 0x3b808081, v5
	v_mul_f32_e32 v10, v69, v5
	v_med3_f32 v7, v7, s19, v229
	v_med3_f32 v8, v8, s19, v229
	v_mov_b32_e32 v5, v1
	v_cvt_pk_fp8_f32 v5, v7, v8
	v_mul_f32_e32 v9, 0x3b808081, v9
	v_mul_f32_e32 v9, v68, v9
	v_med3_f32 v7, v9, s19, v229
	v_med3_f32 v8, v10, s19, v229
	v_cvt_pk_fp8_f32 v5, v7, v8 op_sel:[0,0,1]
	v_add_u32_e32 v7, 0x40000, v0
	global_store_dwordx4 v7, v[2:5], s[48:49]
	s_nop 1
	s_waitcnt vmcnt(7)
	v_cvt_f32_ubyte0_e32 v7, v180
	v_cvt_f32_ubyte1_e32 v8, v180
	v_mul_f32_e32 v7, 0x3b808081, v7
	v_mul_f32_e32 v8, 0x3b808081, v8
	v_cvt_f32_ubyte2_e32 v9, v180
	v_cvt_f32_ubyte3_e32 v2, v180
	v_mul_f32_e32 v7, v62, v7
	v_mul_f32_e32 v8, v63, v8
	v_mul_f32_e32 v2, 0x3b808081, v2
	v_mul_f32_e32 v10, v65, v2
	v_med3_f32 v7, v7, s19, v229
	v_med3_f32 v8, v8, s19, v229
	v_mov_b32_e32 v2, v1
	v_cvt_pk_fp8_f32 v2, v7, v8
	v_mul_f32_e32 v9, 0x3b808081, v9
	v_mul_f32_e32 v9, v64, v9
	v_med3_f32 v7, v9, s19, v229
	v_med3_f32 v8, v10, s19, v229
	v_cvt_pk_fp8_f32 v2, v7, v8 op_sel:[0,0,1]
	v_cvt_f32_ubyte0_e32 v7, v181
	v_cvt_f32_ubyte1_e32 v8, v181
	v_mul_f32_e32 v7, 0x3b808081, v7
	v_mul_f32_e32 v8, 0x3b808081, v8
	v_cvt_f32_ubyte2_e32 v9, v181
	v_cvt_f32_ubyte3_e32 v3, v181
	v_mul_f32_e32 v7, v58, v7
	v_mul_f32_e32 v8, v59, v8
	v_mul_f32_e32 v3, 0x3b808081, v3
	v_mul_f32_e32 v10, v61, v3
	v_med3_f32 v7, v7, s19, v229
	v_med3_f32 v8, v8, s19, v229
	v_mov_b32_e32 v3, v1
	v_cvt_pk_fp8_f32 v3, v7, v8
	v_mul_f32_e32 v9, 0x3b808081, v9
	v_mul_f32_e32 v9, v60, v9
	v_med3_f32 v7, v9, s19, v229
	v_med3_f32 v8, v10, s19, v229
	v_cvt_pk_fp8_f32 v3, v7, v8 op_sel:[0,0,1]
	v_cvt_f32_ubyte0_e32 v7, v182
	v_cvt_f32_ubyte1_e32 v8, v182
	v_mul_f32_e32 v7, 0x3b808081, v7
	v_mul_f32_e32 v8, 0x3b808081, v8
	v_cvt_f32_ubyte2_e32 v9, v182
	v_cvt_f32_ubyte3_e32 v4, v182
	v_mul_f32_e32 v7, v54, v7
	v_mul_f32_e32 v8, v55, v8
	v_mul_f32_e32 v4, 0x3b808081, v4
	v_mul_f32_e32 v10, v57, v4
	v_med3_f32 v7, v7, s19, v229
	v_med3_f32 v8, v8, s19, v229
	v_mov_b32_e32 v4, v1
	v_cvt_pk_fp8_f32 v4, v7, v8
	v_mul_f32_e32 v9, 0x3b808081, v9
	v_mul_f32_e32 v9, v56, v9
	v_med3_f32 v7, v9, s19, v229
	v_med3_f32 v8, v10, s19, v229
	v_cvt_pk_fp8_f32 v4, v7, v8 op_sel:[0,0,1]
	v_cvt_f32_ubyte0_e32 v7, v183
	v_cvt_f32_ubyte1_e32 v8, v183
	v_mul_f32_e32 v7, 0x3b808081, v7
	v_mul_f32_e32 v8, 0x3b808081, v8
	v_cvt_f32_ubyte2_e32 v9, v183
	v_cvt_f32_ubyte3_e32 v5, v183
	v_mul_f32_e32 v7, v50, v7
	v_mul_f32_e32 v8, v51, v8
	v_mul_f32_e32 v5, 0x3b808081, v5
	v_mul_f32_e32 v10, v53, v5
	v_med3_f32 v7, v7, s19, v229
	v_med3_f32 v8, v8, s19, v229
	v_mov_b32_e32 v5, v1
	v_cvt_pk_fp8_f32 v5, v7, v8
	v_mul_f32_e32 v9, 0x3b808081, v9
	v_mul_f32_e32 v9, v52, v9
	v_med3_f32 v7, v9, s19, v229
	v_med3_f32 v8, v10, s19, v229
	v_cvt_pk_fp8_f32 v5, v7, v8 op_sel:[0,0,1]
	v_add_u32_e32 v7, 0x48000, v0
	global_store_dwordx4 v7, v[2:5], s[48:49]
	s_nop 1
	s_waitcnt vmcnt(7)
	v_cvt_f32_ubyte0_e32 v7, v184
	v_cvt_f32_ubyte1_e32 v8, v184
	v_mul_f32_e32 v7, 0x3b808081, v7
	v_mul_f32_e32 v8, 0x3b808081, v8
	v_cvt_f32_ubyte2_e32 v9, v184
	v_cvt_f32_ubyte3_e32 v2, v184
	v_mul_f32_e32 v7, v46, v7
	v_mul_f32_e32 v8, v47, v8
	v_mul_f32_e32 v2, 0x3b808081, v2
	v_mul_f32_e32 v10, v49, v2
	v_med3_f32 v7, v7, s19, v229
	v_med3_f32 v8, v8, s19, v229
	v_mov_b32_e32 v2, v1
	v_cvt_pk_fp8_f32 v2, v7, v8
	v_mul_f32_e32 v9, 0x3b808081, v9
	v_mul_f32_e32 v9, v48, v9
	v_med3_f32 v7, v9, s19, v229
	v_med3_f32 v8, v10, s19, v229
	v_cvt_pk_fp8_f32 v2, v7, v8 op_sel:[0,0,1]
	v_cvt_f32_ubyte0_e32 v7, v185
	v_cvt_f32_ubyte1_e32 v8, v185
	v_mul_f32_e32 v7, 0x3b808081, v7
	v_mul_f32_e32 v8, 0x3b808081, v8
	v_cvt_f32_ubyte2_e32 v9, v185
	v_cvt_f32_ubyte3_e32 v3, v185
	v_mul_f32_e32 v7, v42, v7
	v_mul_f32_e32 v8, v43, v8
	v_mul_f32_e32 v3, 0x3b808081, v3
	v_mul_f32_e32 v10, v45, v3
	v_med3_f32 v7, v7, s19, v229
	v_med3_f32 v8, v8, s19, v229
	v_mov_b32_e32 v3, v1
	v_cvt_pk_fp8_f32 v3, v7, v8
	v_mul_f32_e32 v9, 0x3b808081, v9
	v_mul_f32_e32 v9, v44, v9
	v_med3_f32 v7, v9, s19, v229
	v_med3_f32 v8, v10, s19, v229
	v_cvt_pk_fp8_f32 v3, v7, v8 op_sel:[0,0,1]
	v_cvt_f32_ubyte0_e32 v7, v186
	v_cvt_f32_ubyte1_e32 v8, v186
	v_mul_f32_e32 v7, 0x3b808081, v7
	v_mul_f32_e32 v8, 0x3b808081, v8
	v_cvt_f32_ubyte2_e32 v9, v186
	v_cvt_f32_ubyte3_e32 v4, v186
	v_mul_f32_e32 v7, v38, v7
	v_mul_f32_e32 v8, v39, v8
	v_mul_f32_e32 v4, 0x3b808081, v4
	v_mul_f32_e32 v10, v41, v4
	v_med3_f32 v7, v7, s19, v229
	v_med3_f32 v8, v8, s19, v229
	v_mov_b32_e32 v4, v1
	v_cvt_pk_fp8_f32 v4, v7, v8
	v_mul_f32_e32 v9, 0x3b808081, v9
	v_mul_f32_e32 v9, v40, v9
	v_med3_f32 v7, v9, s19, v229
	v_med3_f32 v8, v10, s19, v229
	v_cvt_pk_fp8_f32 v4, v7, v8 op_sel:[0,0,1]
	v_cvt_f32_ubyte0_e32 v7, v187
	v_cvt_f32_ubyte1_e32 v8, v187
	v_mul_f32_e32 v7, 0x3b808081, v7
	v_mul_f32_e32 v8, 0x3b808081, v8
	v_cvt_f32_ubyte2_e32 v9, v187
	v_cvt_f32_ubyte3_e32 v5, v187
	v_mul_f32_e32 v7, v34, v7
	v_mul_f32_e32 v8, v35, v8
	v_mul_f32_e32 v5, 0x3b808081, v5
	v_mul_f32_e32 v10, v37, v5
	v_med3_f32 v7, v7, s19, v229
	v_med3_f32 v8, v8, s19, v229
	v_mov_b32_e32 v5, v1
	v_cvt_pk_fp8_f32 v5, v7, v8
	v_mul_f32_e32 v9, 0x3b808081, v9
	v_mul_f32_e32 v9, v36, v9
	v_med3_f32 v7, v9, s19, v229
	v_med3_f32 v8, v10, s19, v229
	v_cvt_pk_fp8_f32 v5, v7, v8 op_sel:[0,0,1]
	v_add_u32_e32 v7, 0x50000, v0
	v_add_u32_e32 v0, 0x58000, v0
	global_store_dwordx4 v7, v[2:5], s[48:49]
	s_nop 1
	s_waitcnt vmcnt(7)
	v_cvt_f32_ubyte0_e32 v6, v188
	v_cvt_f32_ubyte1_e32 v7, v188
	v_mul_f32_e32 v6, 0x3b808081, v6
	v_mul_f32_e32 v7, 0x3b808081, v7
	v_cvt_f32_ubyte2_e32 v8, v188
	v_cvt_f32_ubyte3_e32 v2, v188
	v_mul_f32_e32 v6, v30, v6
	v_mul_f32_e32 v7, v31, v7
	v_mul_f32_e32 v2, 0x3b808081, v2
	v_mul_f32_e32 v9, v33, v2
	v_med3_f32 v6, v6, s19, v229
	v_med3_f32 v7, v7, s19, v229
	v_mov_b32_e32 v2, v1
	v_cvt_pk_fp8_f32 v2, v6, v7
	v_mul_f32_e32 v8, 0x3b808081, v8
	v_mul_f32_e32 v8, v32, v8
	v_med3_f32 v6, v8, s19, v229
	v_med3_f32 v7, v9, s19, v229
	v_cvt_pk_fp8_f32 v2, v6, v7 op_sel:[0,0,1]
	v_cvt_f32_ubyte0_e32 v6, v189
	v_cvt_f32_ubyte1_e32 v7, v189
	v_mul_f32_e32 v6, 0x3b808081, v6
	v_mul_f32_e32 v7, 0x3b808081, v7
	v_cvt_f32_ubyte2_e32 v8, v189
	v_cvt_f32_ubyte3_e32 v3, v189
	v_mul_f32_e32 v6, v26, v6
	v_mul_f32_e32 v7, v27, v7
	v_mul_f32_e32 v3, 0x3b808081, v3
	v_mul_f32_e32 v9, v29, v3
	v_med3_f32 v6, v6, s19, v229
	v_med3_f32 v7, v7, s19, v229
	v_mov_b32_e32 v3, v1
	v_cvt_pk_fp8_f32 v3, v6, v7
	v_mul_f32_e32 v8, 0x3b808081, v8
	v_mul_f32_e32 v8, v28, v8
	v_med3_f32 v6, v8, s19, v229
	v_med3_f32 v7, v9, s19, v229
	v_cvt_pk_fp8_f32 v3, v6, v7 op_sel:[0,0,1]
	v_cvt_f32_ubyte0_e32 v6, v190
	v_cvt_f32_ubyte1_e32 v7, v190
	v_mul_f32_e32 v6, 0x3b808081, v6
	v_mul_f32_e32 v7, 0x3b808081, v7
	v_cvt_f32_ubyte2_e32 v8, v190
	v_cvt_f32_ubyte3_e32 v4, v190
	v_mul_f32_e32 v6, v22, v6
	v_mul_f32_e32 v7, v23, v7
	v_mul_f32_e32 v4, 0x3b808081, v4
	v_mul_f32_e32 v9, v25, v4
	v_med3_f32 v6, v6, s19, v229
	v_med3_f32 v7, v7, s19, v229
	v_mov_b32_e32 v4, v1
	v_cvt_pk_fp8_f32 v4, v6, v7
	v_mul_f32_e32 v8, 0x3b808081, v8
	v_mul_f32_e32 v8, v24, v8
	v_med3_f32 v6, v8, s19, v229
	v_med3_f32 v7, v9, s19, v229
	v_cvt_pk_fp8_f32 v4, v6, v7 op_sel:[0,0,1]
	v_cvt_f32_ubyte0_e32 v6, v191
	v_cvt_f32_ubyte1_e32 v7, v191
	v_mul_f32_e32 v6, 0x3b808081, v6
	v_mul_f32_e32 v7, 0x3b808081, v7
	v_cvt_f32_ubyte2_e32 v8, v191
	v_cvt_f32_ubyte3_e32 v5, v191
	v_mul_f32_e32 v6, v18, v6
	v_mul_f32_e32 v7, v19, v7
	v_mul_f32_e32 v5, 0x3b808081, v5
	v_mul_f32_e32 v9, v21, v5
	v_med3_f32 v6, v6, s19, v229
	v_med3_f32 v7, v7, s19, v229
	v_mov_b32_e32 v5, v1
	v_cvt_pk_fp8_f32 v5, v6, v7
	v_mul_f32_e32 v8, 0x3b808081, v8
	v_mul_f32_e32 v8, v20, v8
	v_med3_f32 v6, v8, s19, v229
	v_med3_f32 v7, v9, s19, v229
	v_cvt_pk_fp8_f32 v5, v6, v7 op_sel:[0,0,1]
	global_store_dwordx4 v0, v[2:5], s[48:49]
	s_cbranch_vccnz .LBB0_718
	s_andn2_b64 vcc, exec, s[44:45]
	s_cbranch_vccnz .LBB0_717
	s_barrier
	s_branch .LBB0_717

.LBB0_820:
	v_mov_b32_e32 v0, v183
	s_lshl_b32 s12, s12, 8
	v_readlane_b32 s100, v252, 5
	s_cmp_ge_u32 s100, 4
	s_cbranch_scc0 .Lepi_prio_3
	s_setprio 1
.Lepi_prio_3:
	s_nop 15
	s_nop 15
	s_add_i32 s12, s12, s68
	v_and_or_b32 v2, v0, 15, s12
	s_lshl_b32 s12, s18, 8
	v_ashrrev_i32_e32 v0, 1, v0
	v_and_b32_e32 v0, -8, v0
	v_lshlrev_b32_e32 v2, 11, v2
	s_or_b32 s12, s12, s69
	v_add3_u32 v0, s12, v0, v2
	v_lshlrev_b64 v[10:11], 1, v[0:1]
	v_lshl_add_u64 v[6:7], s[44:45], 0, v[10:11]
	v_add_u32_e32 v220, 0x0, v0
	v_lshlrev_b32_e32 v220, 1, v220
	global_load_dwordx4 v[16:19], v220, s[44:45]
	v_add_u32_e32 v220, 0x0, v0
	v_lshlrev_b32_e32 v220, 1, v220
	global_load_dwordx4 v[20:23], v220, s[44:45] offset:256
	v_add_u32_e32 v220, 0x8000, v0
	v_lshlrev_b32_e32 v220, 1, v220
	global_load_dwordx4 v[24:27], v220, s[44:45]
	v_add_u32_e32 v220, 0x8000, v0
	v_lshlrev_b32_e32 v220, 1, v220
	global_load_dwordx4 v[28:31], v220, s[44:45] offset:256
	v_add_u32_e32 v220, 0x10000, v0
	v_lshlrev_b32_e32 v220, 1, v220
	global_load_dwordx4 v[172:175], v220, s[44:45]
	v_add_u32_e32 v220, 0x10000, v0
	v_lshlrev_b32_e32 v220, 1, v220
	global_load_dwordx4 v[176:179], v220, s[44:45] offset:256
	v_add_u32_e32 v220, 0x18000, v0
	v_lshlrev_b32_e32 v220, 1, v220
	global_load_dwordx4 v[186:189], v220, s[44:45]
	v_add_u32_e32 v220, 0x18000, v0
	v_lshlrev_b32_e32 v220, 1, v220
	global_load_dwordx4 v[190:193], v220, s[44:45] offset:256
	v_add_u32_e32 v220, 0x40000, v0
	v_lshlrev_b32_e32 v220, 1, v220
	global_load_dwordx4 v[194:197], v220, s[44:45]
	v_add_u32_e32 v220, 0x40000, v0
	v_lshlrev_b32_e32 v220, 1, v220
	global_load_dwordx4 v[198:201], v220, s[44:45] offset:256
	v_add_u32_e32 v220, 0x48000, v0
	v_lshlrev_b32_e32 v220, 1, v220
	global_load_dwordx4 v[202:205], v220, s[44:45]
	v_add_u32_e32 v220, 0x48000, v0
	v_lshlrev_b32_e32 v220, 1, v220
	global_load_dwordx4 v[206:209], v220, s[44:45] offset:256
	v_add_u32_e32 v220, 0x50000, v0
	v_lshlrev_b32_e32 v220, 1, v220
	global_load_dwordx4 v[212:215], v220, s[44:45]
	v_add_u32_e32 v220, 0x50000, v0
	v_lshlrev_b32_e32 v220, 1, v220
	global_load_dwordx4 v[216:219], v220, s[44:45] offset:256
	v_lshl_add_u64 v[10:11], s[46:47], 0, v[10:11]
	s_and_b64 vcc, exec, s[38:39]
	s_mov_b64 s[38:39], -1
	s_waitcnt vmcnt(13)
	v_lshlrev_b32_e32 v8, 16, v16
	v_and_b32_e32 v9, 0xffff0000, v16
	v_lshlrev_b32_e32 v2, 16, v17
	v_and_b32_e32 v3, 0xffff0000, v17
	v_lshlrev_b32_e32 v12, 16, v18
	v_and_b32_e32 v13, 0xffff0000, v18
	v_lshlrev_b32_e32 v4, 16, v19
	v_and_b32_e32 v5, 0xffff0000, v19
	v_pk_fma_f32 v[14:15], v[2:3], s[16:17], v[160:161] op_sel_hi:[1,0,1]
	v_pk_fma_f32 v[2:3], v[8:9], s[16:17], v[158:159] op_sel_hi:[1,0,1]
	v_pk_fma_f32 v[8:9], v[4:5], s[16:17], v[156:157] op_sel_hi:[1,0,1]
	v_pk_fma_f32 v[4:5], v[12:13], s[16:17], v[154:155] op_sel_hi:[1,0,1]
	v_cvt_pk_bf16_f32 v2, v2, v3
	v_cvt_pk_bf16_f32 v3, v14, v15
	v_mov_b32_e32 v13, v1
	v_cvt_pk_bf16_f32 v4, v4, v5
	v_cvt_pk_bf16_f32 v5, v8, v9
	v_add_u32_e32 v220, 0x58000, v0
	v_lshlrev_b32_e32 v220, 1, v220
	global_load_dwordx4 v[16:19], v220, s[44:45]
	v_add_u32_e32 v12, 0x8000, v0
	global_store_dwordx4 v[10:11], v[2:5], off
	v_lshlrev_b64 v[12:13], 1, v[12:13]
	v_lshl_add_u64 v[14:15], s[44:45], 0, v[12:13]
	v_lshl_add_u64 v[12:13], s[46:47], 0, v[12:13]
	s_waitcnt vmcnt(14)
	v_lshlrev_b32_e32 v2, 16, v20
	v_and_b32_e32 v3, 0xffff0000, v20
	v_lshlrev_b32_e32 v4, 16, v21
	v_and_b32_e32 v5, 0xffff0000, v21
	v_lshlrev_b32_e32 v6, 16, v22
	v_and_b32_e32 v7, 0xffff0000, v22
	v_lshlrev_b32_e32 v8, 16, v23
	v_and_b32_e32 v9, 0xffff0000, v23
	v_pk_fma_f32 v[4:5], v[4:5], s[16:17], v[152:153] op_sel_hi:[1,0,1]
	v_pk_fma_f32 v[2:3], v[2:3], s[16:17], v[150:151] op_sel_hi:[1,0,1]
	v_pk_fma_f32 v[8:9], v[8:9], s[16:17], v[148:149] op_sel_hi:[1,0,1]
	v_pk_fma_f32 v[6:7], v[6:7], s[16:17], v[146:147] op_sel_hi:[1,0,1]
	v_cvt_pk_bf16_f32 v2, v2, v3
	v_cvt_pk_bf16_f32 v3, v4, v5
	s_nop 0
	v_cvt_pk_bf16_f32 v4, v6, v7
	v_cvt_pk_bf16_f32 v5, v8, v9
	global_store_dwordx4 v[10:11], v[2:5], off offset:256
	v_add_u32_e32 v220, 0x58000, v0
	v_lshlrev_b32_e32 v220, 1, v220
	global_load_dwordx4 v[20:23], v220, s[44:45] offset:256
	s_waitcnt vmcnt(15)
	v_lshlrev_b32_e32 v6, 16, v24
	v_and_b32_e32 v7, 0xffff0000, v24
	v_lshlrev_b32_e32 v2, 16, v25
	v_and_b32_e32 v3, 0xffff0000, v25
	v_lshlrev_b32_e32 v8, 16, v26
	v_and_b32_e32 v9, 0xffff0000, v26
	v_lshlrev_b32_e32 v4, 16, v27
	v_and_b32_e32 v5, 0xffff0000, v27
	v_pk_fma_f32 v[10:11], v[2:3], s[16:17], v[144:145] op_sel_hi:[1,0,1]
	v_pk_fma_f32 v[2:3], v[6:7], s[16:17], v[142:143] op_sel_hi:[1,0,1]
	v_pk_fma_f32 v[6:7], v[4:5], s[16:17], v[140:141] op_sel_hi:[1,0,1]
	v_pk_fma_f32 v[4:5], v[8:9], s[16:17], v[138:139] op_sel_hi:[1,0,1]
	v_cvt_pk_bf16_f32 v2, v2, v3
	v_cvt_pk_bf16_f32 v3, v10, v11
	v_mov_b32_e32 v11, v1
	v_cvt_pk_bf16_f32 v4, v4, v5
	v_cvt_pk_bf16_f32 v5, v6, v7
	v_add_u32_e32 v10, 0x10000, v0
	global_store_dwordx4 v[12:13], v[2:5], off
	v_lshlrev_b64 v[10:11], 1, v[10:11]
	v_lshl_add_u64 v[14:15], s[44:45], 0, v[10:11]
	v_lshl_add_u64 v[10:11], s[46:47], 0, v[10:11]
	s_waitcnt vmcnt(15)
	v_lshlrev_b32_e32 v2, 16, v28
	v_and_b32_e32 v3, 0xffff0000, v28
	v_lshlrev_b32_e32 v4, 16, v29
	v_and_b32_e32 v5, 0xffff0000, v29
	v_lshlrev_b32_e32 v6, 16, v30
	v_and_b32_e32 v7, 0xffff0000, v30
	v_lshlrev_b32_e32 v8, 16, v31
	v_and_b32_e32 v9, 0xffff0000, v31
	v_pk_fma_f32 v[4:5], v[4:5], s[16:17], v[136:137] op_sel_hi:[1,0,1]
	v_pk_fma_f32 v[2:3], v[2:3], s[16:17], v[134:135] op_sel_hi:[1,0,1]
	v_pk_fma_f32 v[8:9], v[8:9], s[16:17], v[132:133] op_sel_hi:[1,0,1]
	v_pk_fma_f32 v[6:7], v[6:7], s[16:17], v[130:131] op_sel_hi:[1,0,1]
	v_cvt_pk_bf16_f32 v2, v2, v3
	v_cvt_pk_bf16_f32 v3, v4, v5
	s_nop 0
	v_cvt_pk_bf16_f32 v4, v6, v7
	v_cvt_pk_bf16_f32 v5, v8, v9
	global_store_dwordx4 v[12:13], v[2:5], off offset:256
	s_waitcnt vmcnt(15)
	v_lshlrev_b32_e32 v6, 16, v172
	v_and_b32_e32 v7, 0xffff0000, v172
	v_lshlrev_b32_e32 v2, 16, v173
	v_and_b32_e32 v3, 0xffff0000, v173
	v_lshlrev_b32_e32 v8, 16, v174
	v_and_b32_e32 v9, 0xffff0000, v174
	v_lshlrev_b32_e32 v4, 16, v175
	v_and_b32_e32 v5, 0xffff0000, v175
	v_pk_fma_f32 v[12:13], v[2:3], s[16:17], v[128:129] op_sel_hi:[1,0,1]
	v_pk_fma_f32 v[2:3], v[6:7], s[16:17], v[126:127] op_sel_hi:[1,0,1]
	v_pk_fma_f32 v[6:7], v[4:5], s[16:17], v[124:125] op_sel_hi:[1,0,1]
	v_pk_fma_f32 v[4:5], v[8:9], s[16:17], v[122:123] op_sel_hi:[1,0,1]
	v_cvt_pk_bf16_f32 v2, v2, v3
	v_cvt_pk_bf16_f32 v3, v12, v13
	v_mov_b32_e32 v13, v1
	v_cvt_pk_bf16_f32 v4, v4, v5
	v_cvt_pk_bf16_f32 v5, v6, v7
	v_add_u32_e32 v12, 0x18000, v0
	global_store_dwordx4 v[10:11], v[2:5], off
	v_lshlrev_b64 v[12:13], 1, v[12:13]
	v_lshl_add_u64 v[14:15], s[44:45], 0, v[12:13]
	v_lshl_add_u64 v[12:13], s[46:47], 0, v[12:13]
	s_waitcnt vmcnt(15)
	v_lshlrev_b32_e32 v2, 16, v176
	v_and_b32_e32 v3, 0xffff0000, v176
	v_lshlrev_b32_e32 v4, 16, v177
	v_and_b32_e32 v5, 0xffff0000, v177
	v_lshlrev_b32_e32 v6, 16, v178
	v_and_b32_e32 v7, 0xffff0000, v178
	v_lshlrev_b32_e32 v8, 16, v179
	v_and_b32_e32 v9, 0xffff0000, v179
	v_pk_fma_f32 v[4:5], v[4:5], s[16:17], v[120:121] op_sel_hi:[1,0,1]
	v_pk_fma_f32 v[2:3], v[2:3], s[16:17], v[118:119] op_sel_hi:[1,0,1]
	v_pk_fma_f32 v[8:9], v[8:9], s[16:17], v[116:117] op_sel_hi:[1,0,1]
	v_pk_fma_f32 v[6:7], v[6:7], s[16:17], v[114:115] op_sel_hi:[1,0,1]
	v_cvt_pk_bf16_f32 v2, v2, v3
	v_cvt_pk_bf16_f32 v3, v4, v5
	s_nop 0
	v_cvt_pk_bf16_f32 v4, v6, v7
	v_cvt_pk_bf16_f32 v5, v8, v9
	global_store_dwordx4 v[10:11], v[2:5], off offset:256
	s_waitcnt vmcnt(15)
	v_lshlrev_b32_e32 v6, 16, v186
	v_and_b32_e32 v7, 0xffff0000, v186
	v_lshlrev_b32_e32 v2, 16, v187
	v_and_b32_e32 v3, 0xffff0000, v187
	v_lshlrev_b32_e32 v8, 16, v188
	v_and_b32_e32 v9, 0xffff0000, v188
	v_lshlrev_b32_e32 v4, 16, v189
	v_and_b32_e32 v5, 0xffff0000, v189
	v_pk_fma_f32 v[10:11], v[2:3], s[16:17], v[112:113] op_sel_hi:[1,0,1]
	v_pk_fma_f32 v[2:3], v[6:7], s[16:17], v[110:111] op_sel_hi:[1,0,1]
	v_pk_fma_f32 v[6:7], v[4:5], s[16:17], v[108:109] op_sel_hi:[1,0,1]
	v_pk_fma_f32 v[4:5], v[8:9], s[16:17], v[106:107] op_sel_hi:[1,0,1]
	v_cvt_pk_bf16_f32 v2, v2, v3
	v_cvt_pk_bf16_f32 v3, v10, v11
	v_mov_b32_e32 v11, v1
	v_cvt_pk_bf16_f32 v4, v4, v5
	v_cvt_pk_bf16_f32 v5, v6, v7
	v_add_u32_e32 v10, 0x40000, v0
	global_store_dwordx4 v[12:13], v[2:5], off
	v_lshlrev_b64 v[10:11], 1, v[10:11]
	v_lshl_add_u64 v[14:15], s[44:45], 0, v[10:11]
	v_lshl_add_u64 v[10:11], s[46:47], 0, v[10:11]
	s_waitcnt vmcnt(15)
	v_lshlrev_b32_e32 v2, 16, v190
	v_and_b32_e32 v3, 0xffff0000, v190
	v_lshlrev_b32_e32 v4, 16, v191
	v_and_b32_e32 v5, 0xffff0000, v191
	v_lshlrev_b32_e32 v6, 16, v192
	v_and_b32_e32 v7, 0xffff0000, v192
	v_lshlrev_b32_e32 v8, 16, v193
	v_and_b32_e32 v9, 0xffff0000, v193
	v_pk_fma_f32 v[4:5], v[4:5], s[16:17], v[104:105] op_sel_hi:[1,0,1]
	v_pk_fma_f32 v[2:3], v[2:3], s[16:17], v[102:103] op_sel_hi:[1,0,1]
	v_pk_fma_f32 v[8:9], v[8:9], s[16:17], v[100:101] op_sel_hi:[1,0,1]
	v_pk_fma_f32 v[6:7], v[6:7], s[16:17], v[98:99] op_sel_hi:[1,0,1]
	v_cvt_pk_bf16_f32 v2, v2, v3
	v_cvt_pk_bf16_f32 v3, v4, v5
	s_nop 0
	v_cvt_pk_bf16_f32 v4, v6, v7
	v_cvt_pk_bf16_f32 v5, v8, v9
	global_store_dwordx4 v[12:13], v[2:5], off offset:256
	s_waitcnt vmcnt(15)
	v_lshlrev_b32_e32 v6, 16, v194
	v_and_b32_e32 v7, 0xffff0000, v194
	v_lshlrev_b32_e32 v2, 16, v195
	v_and_b32_e32 v3, 0xffff0000, v195
	v_lshlrev_b32_e32 v8, 16, v196
	v_and_b32_e32 v9, 0xffff0000, v196
	v_lshlrev_b32_e32 v4, 16, v197
	v_and_b32_e32 v5, 0xffff0000, v197
	v_pk_fma_f32 v[12:13], v[2:3], s[16:17], v[96:97] op_sel_hi:[1,0,1]
	v_pk_fma_f32 v[2:3], v[6:7], s[16:17], v[94:95] op_sel_hi:[1,0,1]
	v_pk_fma_f32 v[6:7], v[4:5], s[16:17], v[92:93] op_sel_hi:[1,0,1]
	v_pk_fma_f32 v[4:5], v[8:9], s[16:17], v[90:91] op_sel_hi:[1,0,1]
	v_cvt_pk_bf16_f32 v2, v2, v3
	v_cvt_pk_bf16_f32 v3, v12, v13
	v_mov_b32_e32 v13, v1
	v_cvt_pk_bf16_f32 v4, v4, v5
	v_cvt_pk_bf16_f32 v5, v6, v7
	v_add_u32_e32 v12, 0x48000, v0
	global_store_dwordx4 v[10:11], v[2:5], off
	v_lshlrev_b64 v[12:13], 1, v[12:13]
	v_lshl_add_u64 v[14:15], s[44:45], 0, v[12:13]
	v_lshl_add_u64 v[12:13], s[46:47], 0, v[12:13]
	s_waitcnt vmcnt(15)
	v_lshlrev_b32_e32 v2, 16, v198
	v_and_b32_e32 v3, 0xffff0000, v198
	v_lshlrev_b32_e32 v4, 16, v199
	v_and_b32_e32 v5, 0xffff0000, v199
	v_lshlrev_b32_e32 v6, 16, v200
	v_and_b32_e32 v7, 0xffff0000, v200
	v_lshlrev_b32_e32 v8, 16, v201
	v_and_b32_e32 v9, 0xffff0000, v201
	v_pk_fma_f32 v[4:5], v[4:5], s[16:17], v[88:89] op_sel_hi:[1,0,1]
	v_pk_fma_f32 v[2:3], v[2:3], s[16:17], v[86:87] op_sel_hi:[1,0,1]
	v_pk_fma_f32 v[8:9], v[8:9], s[16:17], v[84:85] op_sel_hi:[1,0,1]
	v_pk_fma_f32 v[6:7], v[6:7], s[16:17], v[82:83] op_sel_hi:[1,0,1]
	v_cvt_pk_bf16_f32 v2, v2, v3
	v_cvt_pk_bf16_f32 v3, v4, v5
	s_nop 0
	v_cvt_pk_bf16_f32 v4, v6, v7
	v_cvt_pk_bf16_f32 v5, v8, v9
	global_store_dwordx4 v[10:11], v[2:5], off offset:256
	s_waitcnt vmcnt(15)
	v_lshlrev_b32_e32 v6, 16, v202
	v_and_b32_e32 v7, 0xffff0000, v202
	v_lshlrev_b32_e32 v2, 16, v203
	v_and_b32_e32 v3, 0xffff0000, v203
	v_lshlrev_b32_e32 v8, 16, v204
	v_and_b32_e32 v9, 0xffff0000, v204
	v_lshlrev_b32_e32 v4, 16, v205
	v_and_b32_e32 v5, 0xffff0000, v205
	v_pk_fma_f32 v[10:11], v[2:3], s[16:17], v[80:81] op_sel_hi:[1,0,1]
	v_pk_fma_f32 v[2:3], v[6:7], s[16:17], v[78:79] op_sel_hi:[1,0,1]
	v_pk_fma_f32 v[6:7], v[4:5], s[16:17], v[76:77] op_sel_hi:[1,0,1]
	v_pk_fma_f32 v[4:5], v[8:9], s[16:17], v[74:75] op_sel_hi:[1,0,1]
	v_cvt_pk_bf16_f32 v2, v2, v3
	v_cvt_pk_bf16_f32 v3, v10, v11
	v_mov_b32_e32 v11, v1
	v_cvt_pk_bf16_f32 v4, v4, v5
	v_cvt_pk_bf16_f32 v5, v6, v7
	v_add_u32_e32 v10, 0x50000, v0
	global_store_dwordx4 v[12:13], v[2:5], off
	v_lshlrev_b64 v[10:11], 1, v[10:11]
	v_lshl_add_u64 v[14:15], s[44:45], 0, v[10:11]
	v_lshl_add_u64 v[10:11], s[46:47], 0, v[10:11]
	v_add_u32_e32 v0, 0x58000, v0
	s_waitcnt vmcnt(15)
	v_lshlrev_b32_e32 v2, 16, v206
	v_and_b32_e32 v3, 0xffff0000, v206
	v_lshlrev_b32_e32 v4, 16, v207
	v_and_b32_e32 v5, 0xffff0000, v207
	v_lshlrev_b32_e32 v6, 16, v208
	v_and_b32_e32 v7, 0xffff0000, v208
	v_lshlrev_b32_e32 v8, 16, v209
	v_and_b32_e32 v9, 0xffff0000, v209
	v_pk_fma_f32 v[4:5], v[4:5], s[16:17], v[72:73] op_sel_hi:[1,0,1]
	v_pk_fma_f32 v[2:3], v[2:3], s[16:17], v[70:71] op_sel_hi:[1,0,1]
	v_pk_fma_f32 v[8:9], v[8:9], s[16:17], v[68:69] op_sel_hi:[1,0,1]
	v_pk_fma_f32 v[6:7], v[6:7], s[16:17], v[66:67] op_sel_hi:[1,0,1]
	v_cvt_pk_bf16_f32 v2, v2, v3
	v_cvt_pk_bf16_f32 v3, v4, v5
	s_nop 0
	v_cvt_pk_bf16_f32 v4, v6, v7
	v_cvt_pk_bf16_f32 v5, v8, v9
	global_store_dwordx4 v[12:13], v[2:5], off offset:256
	s_waitcnt vmcnt(15)
	v_lshlrev_b32_e32 v6, 16, v212
	v_and_b32_e32 v7, 0xffff0000, v212
	v_lshlrev_b32_e32 v2, 16, v213
	v_and_b32_e32 v3, 0xffff0000, v213
	v_lshlrev_b32_e32 v8, 16, v214
	v_and_b32_e32 v9, 0xffff0000, v214
	v_lshlrev_b32_e32 v4, 16, v215
	v_and_b32_e32 v5, 0xffff0000, v215
	v_pk_fma_f32 v[12:13], v[2:3], s[16:17], v[64:65] op_sel_hi:[1,0,1]
	v_pk_fma_f32 v[2:3], v[6:7], s[16:17], v[62:63] op_sel_hi:[1,0,1]
	v_pk_fma_f32 v[6:7], v[4:5], s[16:17], v[60:61] op_sel_hi:[1,0,1]
	v_pk_fma_f32 v[4:5], v[8:9], s[16:17], v[58:59] op_sel_hi:[1,0,1]
	v_cvt_pk_bf16_f32 v2, v2, v3
	v_cvt_pk_bf16_f32 v3, v12, v13
	v_lshlrev_b64 v[12:13], 1, v[0:1]
	v_cvt_pk_bf16_f32 v4, v4, v5
	v_cvt_pk_bf16_f32 v5, v6, v7
	v_lshl_add_u64 v[14:15], s[44:45], 0, v[12:13]
	global_store_dwordx4 v[10:11], v[2:5], off
	s_waitcnt vmcnt(15)
	s_nop 0
	v_lshlrev_b32_e32 v2, 16, v216
	v_and_b32_e32 v3, 0xffff0000, v216
	v_lshlrev_b32_e32 v4, 16, v217
	v_and_b32_e32 v5, 0xffff0000, v217
	v_lshlrev_b32_e32 v6, 16, v218
	v_and_b32_e32 v7, 0xffff0000, v218
	v_lshlrev_b32_e32 v8, 16, v219
	v_and_b32_e32 v9, 0xffff0000, v219
	v_pk_fma_f32 v[4:5], v[4:5], s[16:17], v[56:57] op_sel_hi:[1,0,1]
	v_pk_fma_f32 v[2:3], v[2:3], s[16:17], v[54:55] op_sel_hi:[1,0,1]
	v_pk_fma_f32 v[8:9], v[8:9], s[16:17], v[52:53] op_sel_hi:[1,0,1]
	v_pk_fma_f32 v[6:7], v[6:7], s[16:17], v[50:51] op_sel_hi:[1,0,1]
	v_cvt_pk_bf16_f32 v2, v2, v3
	v_cvt_pk_bf16_f32 v3, v4, v5
	s_nop 0
	v_cvt_pk_bf16_f32 v4, v6, v7
	v_cvt_pk_bf16_f32 v5, v8, v9
	global_store_dwordx4 v[10:11], v[2:5], off offset:256
	s_waitcnt vmcnt(15)
	v_lshlrev_b32_e32 v6, 16, v16
	v_and_b32_e32 v7, 0xffff0000, v16
	v_lshlrev_b32_e32 v2, 16, v17
	v_and_b32_e32 v3, 0xffff0000, v17
	v_lshlrev_b32_e32 v8, 16, v18
	v_and_b32_e32 v9, 0xffff0000, v18
	v_lshlrev_b32_e32 v4, 16, v19
	v_and_b32_e32 v5, 0xffff0000, v19
	v_pk_fma_f32 v[10:11], v[2:3], s[16:17], v[48:49] op_sel_hi:[1,0,1]
	v_pk_fma_f32 v[2:3], v[6:7], s[16:17], v[46:47] op_sel_hi:[1,0,1]
	v_pk_fma_f32 v[6:7], v[4:5], s[16:17], v[44:45] op_sel_hi:[1,0,1]
	v_pk_fma_f32 v[4:5], v[8:9], s[16:17], v[42:43] op_sel_hi:[1,0,1]
	v_cvt_pk_bf16_f32 v2, v2, v3
	v_cvt_pk_bf16_f32 v3, v10, v11
	v_lshl_add_u64 v[10:11], s[46:47], 0, v[12:13]
	v_cvt_pk_bf16_f32 v4, v4, v5
	v_cvt_pk_bf16_f32 v5, v6, v7
	s_nop 0
	global_store_dwordx4 v[10:11], v[2:5], off
	s_waitcnt vmcnt(13)
	s_nop 0
	v_lshlrev_b32_e32 v2, 16, v20
	v_and_b32_e32 v3, 0xffff0000, v20
	v_lshlrev_b32_e32 v4, 16, v21
	v_and_b32_e32 v5, 0xffff0000, v21
	v_lshlrev_b32_e32 v6, 16, v22
	v_and_b32_e32 v7, 0xffff0000, v22
	v_lshlrev_b32_e32 v8, 16, v23
	v_and_b32_e32 v9, 0xffff0000, v23
	v_pk_fma_f32 v[4:5], v[4:5], s[16:17], v[40:41] op_sel_hi:[1,0,1]
	v_pk_fma_f32 v[2:3], v[2:3], s[16:17], v[38:39] op_sel_hi:[1,0,1]
	v_pk_fma_f32 v[8:9], v[8:9], s[16:17], v[36:37] op_sel_hi:[1,0,1]
	v_pk_fma_f32 v[6:7], v[6:7], s[16:17], v[34:35] op_sel_hi:[1,0,1]
	v_cvt_pk_bf16_f32 v2, v2, v3
	v_cvt_pk_bf16_f32 v3, v4, v5
	s_nop 0
	v_cvt_pk_bf16_f32 v4, v6, v7
	v_cvt_pk_bf16_f32 v5, v8, v9
	global_store_dwordx4 v[10:11], v[2:5], off offset:256
	s_cbranch_vccnz .LBB0_804
	s_andn2_b64 vcc, exec, s[42:43]
	s_cbranch_vccnz .LBB0_803
	s_barrier
	s_branch .LBB0_803

.LBB0_1197:
	v_mul_f32_e32 v8, 0xbfb8aa3b, v161
	v_exp_f32_e32 v8, v8
	v_mul_f32_e32 v9, 0xbfb8aa3b, v150
	v_exp_f32_e32 v9, v9
	v_mul_f32_e32 v10, 0xbfb8aa3b, v151
	v_add_f32_e32 v8, 1.0, v8
	v_rcp_f32_e32 v8, v8
	v_add_f32_e32 v9, 1.0, v9
	v_rcp_f32_e32 v9, v9
	v_mov_b32_e32 v0, v177
	s_lshl_b32 s56, s82, 8
	v_exp_f32_e32 v10, v10
	v_readlane_b32 s100, v252, 5
	s_cmp_ge_u32 s100, 4
	s_cbranch_scc0 .Lepi_prio_4
	s_setprio 1
.Lepi_prio_4:
	s_nop 15
	s_nop 15
	s_add_i32 s56, s56, s75
	s_lshl_b32 s12, s12, 7
	v_and_or_b32 v6, v0, 15, s56
	s_and_b32 s12, s12, 0x180
	v_ashrrev_i32_e32 v0, 1, v0
	v_mul_f32_e32 v8, v161, v8
	s_or_b32 s12, s12, s70
	v_and_b32_e32 v0, -8, v0
	v_mul_f32_e32 v11, v157, v8
	v_mul_f32_e32 v8, v150, v9
	v_add_u32_e32 v4, s12, v0
	v_mul_f32_e32 v0, 0xbfb8aa3b, v158
	v_mul_f32_e32 v2, 0xbfb8aa3b, v159
	v_mul_f32_e32 v9, v146, v8
	v_add_f32_e32 v8, 1.0, v10
	v_mul_f32_e32 v10, 0xbfb8aa3b, v152
	v_exp_f32_e32 v0, v0
	v_exp_f32_e32 v2, v2
	v_exp_f32_e32 v10, v10
	v_mul_f32_e32 v12, 0xbfb8aa3b, v153
	v_exp_f32_e32 v12, v12
	v_mul_f32_e32 v3, 0xbfb8aa3b, v160
	v_add_f32_e32 v0, 1.0, v0
	v_add_f32_e32 v2, 1.0, v2
	v_exp_f32_e32 v3, v3
	v_rcp_f32_e32 v8, v8
	v_add_f32_e32 v10, 1.0, v10
	v_rcp_f32_e32 v0, v0
	v_rcp_f32_e32 v2, v2
	v_rcp_f32_e32 v10, v10
	v_add_f32_e32 v12, 1.0, v12
	v_rcp_f32_e32 v12, v12
	v_add_f32_e32 v3, 1.0, v3
	v_mul_f32_e32 v8, v151, v8
	v_mul_f32_e32 v0, v158, v0
	v_mul_f32_e32 v2, v159, v2
	v_rcp_f32_e32 v3, v3
	v_mul_f32_e32 v13, v147, v8
	v_mul_f32_e32 v8, v152, v10
	v_mul_f32_e32 v0, v154, v0
	v_mul_f32_e32 v2, v155, v2
	v_mul_f32_e32 v10, v148, v8
	v_mul_f32_e32 v8, v153, v12
	v_mul_f32_e32 v12, v149, v8
	v_med3_f32 v0, v0, s19, v229
	v_med3_f32 v2, v2, s19, v229
	v_mov_b32_e32 v8, v1
	v_cvt_pk_fp8_f32 v8, v0, v2
	v_mul_f32_e32 v3, v160, v3
	v_mul_f32_e32 v3, v156, v3
	v_med3_f32 v0, v3, s19, v229
	v_med3_f32 v2, v11, s19, v229
	v_med3_f32 v3, v9, s19, v229
	v_med3_f32 v11, v13, s19, v229
	v_mov_b32_e32 v9, v1
	v_cvt_pk_fp8_f32 v8, v0, v2 op_sel:[0,0,1]
	v_med3_f32 v0, v10, s19, v229
	v_mul_f32_e32 v10, 0xbfb8aa3b, v144
	v_cvt_pk_fp8_f32 v9, v3, v11
	v_exp_f32_e32 v10, v10
	v_mul_f32_e32 v11, 0xbfb8aa3b, v145
	v_exp_f32_e32 v11, v11
	v_med3_f32 v2, v12, s19, v229
	v_add_f32_e32 v10, 1.0, v10
	v_rcp_f32_e32 v10, v10
	v_add_f32_e32 v11, 1.0, v11
	v_mul_f32_e32 v12, 0xbfb8aa3b, v134
	v_rcp_f32_e32 v11, v11
	v_exp_f32_e32 v12, v12
	v_mul_f32_e32 v10, v144, v10
	v_mul_f32_e32 v13, v140, v10
	v_mul_f32_e32 v10, v145, v11
	v_add_f32_e32 v11, 1.0, v12
	v_rcp_f32_e32 v11, v11
	v_mul_f32_e32 v12, 0xbfb8aa3b, v135
	v_exp_f32_e32 v12, v12
	v_ashrrev_i32_e32 v7, 31, v6
	v_mul_f32_e32 v14, v141, v10
	v_mul_f32_e32 v10, v134, v11
	v_cvt_pk_fp8_f32 v9, v0, v2 op_sel:[0,0,1]
	v_lshlrev_b64 v[2:3], 9, v[6:7]
	v_mul_f32_e32 v0, 0xbfb8aa3b, v142
	v_mul_f32_e32 v7, 0xbfb8aa3b, v143
	v_mul_f32_e32 v11, v130, v10
	v_add_f32_e32 v10, 1.0, v12
	v_mul_f32_e32 v12, 0xbfb8aa3b, v136
	v_exp_f32_e32 v0, v0
	v_exp_f32_e32 v7, v7
	v_exp_f32_e32 v12, v12
	v_mul_f32_e32 v15, 0xbfb8aa3b, v137
	v_exp_f32_e32 v15, v15
	v_add_f32_e32 v0, 1.0, v0
	v_add_f32_e32 v7, 1.0, v7
	v_rcp_f32_e32 v10, v10
	v_add_f32_e32 v12, 1.0, v12
	v_rcp_f32_e32 v0, v0
	v_rcp_f32_e32 v7, v7
	v_rcp_f32_e32 v12, v12
	v_add_f32_e32 v15, 1.0, v15
	v_rcp_f32_e32 v15, v15
	v_mul_f32_e32 v10, v135, v10
	v_mul_f32_e32 v0, v142, v0
	v_mul_f32_e32 v7, v143, v7
	v_mul_f32_e32 v16, v131, v10
	v_mul_f32_e32 v10, v136, v12
	v_mul_f32_e32 v0, v138, v0
	v_mul_f32_e32 v7, v139, v7
	v_mul_f32_e32 v12, v132, v10
	v_mul_f32_e32 v10, v137, v15
	v_mul_f32_e32 v15, v133, v10
	v_med3_f32 v0, v0, s19, v229
	v_med3_f32 v7, v7, s19, v229
	v_mov_b32_e32 v10, v1
	v_cvt_pk_fp8_f32 v10, v0, v7
	v_med3_f32 v0, v13, s19, v229
	v_med3_f32 v7, v14, s19, v229
	v_med3_f32 v13, v11, s19, v229
	v_med3_f32 v14, v16, s19, v229
	v_mov_b32_e32 v11, v1
	v_cvt_pk_fp8_f32 v11, v13, v14
	v_ashrrev_i32_e32 v5, 31, v4
	v_lshl_add_u64 v[2:3], s[46:47], 0, v[2:3]
	v_lshl_add_u64 v[2:3], v[2:3], 0, v[4:5]
	global_store_dwordx2 v[2:3], v[8:9], off
	v_or_b32_e32 v8, 16, v6
	v_cvt_pk_fp8_f32 v10, v0, v7 op_sel:[0,0,1]
	v_med3_f32 v0, v12, s19, v229
	v_med3_f32 v7, v15, s19, v229
	v_ashrrev_i32_e32 v9, 31, v8
	v_cvt_pk_fp8_f32 v11, v0, v7 op_sel:[0,0,1]
	v_lshlrev_b64 v[8:9], 9, v[8:9]
	v_lshl_add_u64 v[8:9], s[46:47], 0, v[8:9]
	v_lshl_add_u64 v[8:9], v[8:9], 0, v[4:5]
	global_store_dwordx2 v[8:9], v[10:11], off
	v_mul_f32_e32 v10, 0xbfb8aa3b, v128
	v_exp_f32_e32 v10, v10
	v_mul_f32_e32 v11, 0xbfb8aa3b, v129
	v_exp_f32_e32 v11, v11
	v_mul_f32_e32 v12, 0xbfb8aa3b, v118
	v_add_f32_e32 v10, 1.0, v10
	v_rcp_f32_e32 v10, v10
	v_add_f32_e32 v11, 1.0, v11
	v_rcp_f32_e32 v11, v11
	v_exp_f32_e32 v12, v12
	v_mul_f32_e32 v10, v128, v10
	v_mul_f32_e32 v13, v124, v10
	v_mul_f32_e32 v10, v129, v11
	v_add_f32_e32 v11, 1.0, v12
	v_rcp_f32_e32 v11, v11
	v_mul_f32_e32 v12, 0xbfb8aa3b, v119
	v_exp_f32_e32 v12, v12
	v_mul_f32_e32 v14, v125, v10
	v_mul_f32_e32 v10, v118, v11
	v_mul_f32_e32 v0, 0xbfb8aa3b, v126
	v_mul_f32_e32 v7, 0xbfb8aa3b, v127
	v_mul_f32_e32 v11, v114, v10
	v_add_f32_e32 v10, 1.0, v12
	v_mul_f32_e32 v12, 0xbfb8aa3b, v120
	v_exp_f32_e32 v0, v0
	v_exp_f32_e32 v7, v7
	v_exp_f32_e32 v12, v12
	v_mul_f32_e32 v15, 0xbfb8aa3b, v121
	v_exp_f32_e32 v15, v15
	v_add_f32_e32 v0, 1.0, v0
	v_add_f32_e32 v7, 1.0, v7
	v_rcp_f32_e32 v10, v10
	v_add_f32_e32 v12, 1.0, v12
	v_rcp_f32_e32 v0, v0
	v_rcp_f32_e32 v7, v7
	v_rcp_f32_e32 v12, v12
	v_add_f32_e32 v15, 1.0, v15
	v_rcp_f32_e32 v15, v15
	v_mul_f32_e32 v10, v119, v10
	v_mul_f32_e32 v0, v126, v0
	v_mul_f32_e32 v7, v127, v7
	v_mul_f32_e32 v16, v115, v10
	v_mul_f32_e32 v10, v120, v12
	v_mul_f32_e32 v0, v122, v0
	v_mul_f32_e32 v7, v123, v7
	v_mul_f32_e32 v12, v116, v10
	v_mul_f32_e32 v10, v121, v15
	v_mul_f32_e32 v15, v117, v10
	v_med3_f32 v0, v0, s19, v229
	v_med3_f32 v7, v7, s19, v229
	v_mov_b32_e32 v10, v1
	v_cvt_pk_fp8_f32 v10, v0, v7
	v_med3_f32 v0, v13, s19, v229
	v_med3_f32 v7, v14, s19, v229
	v_med3_f32 v13, v11, s19, v229
	v_med3_f32 v14, v16, s19, v229
	v_mov_b32_e32 v11, v1
	v_cvt_pk_fp8_f32 v11, v13, v14
	v_or_b32_e32 v8, 32, v6
	v_cvt_pk_fp8_f32 v10, v0, v7 op_sel:[0,0,1]
	v_med3_f32 v0, v12, s19, v229
	v_med3_f32 v7, v15, s19, v229
	v_ashrrev_i32_e32 v9, 31, v8
	v_cvt_pk_fp8_f32 v11, v0, v7 op_sel:[0,0,1]
	v_lshlrev_b64 v[8:9], 9, v[8:9]
	v_lshl_add_u64 v[8:9], s[46:47], 0, v[8:9]
	v_lshl_add_u64 v[8:9], v[8:9], 0, v[4:5]
	global_store_dwordx2 v[8:9], v[10:11], off
	v_mul_f32_e32 v0, 0xbfb8aa3b, v110
	v_mul_f32_e32 v8, 0xbfb8aa3b, v111
	v_exp_f32_e32 v0, v0
	v_exp_f32_e32 v8, v8
	v_mul_f32_e32 v9, 0xbfb8aa3b, v112
	v_mul_f32_e32 v10, 0xbfb8aa3b, v113
	v_add_f32_e32 v0, 1.0, v0
	v_add_f32_e32 v8, 1.0, v8
	v_exp_f32_e32 v9, v9
	v_exp_f32_e32 v10, v10
	v_mul_f32_e32 v11, 0xbfb8aa3b, v102
	v_mul_f32_e32 v12, 0xbfb8aa3b, v103
	v_rcp_f32_e32 v0, v0
	v_rcp_f32_e32 v8, v8
	v_exp_f32_e32 v11, v11
	v_exp_f32_e32 v12, v12
	v_add_f32_e32 v9, 1.0, v9
	v_add_f32_e32 v10, 1.0, v10
	v_mul_f32_e32 v13, 0xbfb8aa3b, v104
	v_mul_f32_e32 v14, 0xbfb8aa3b, v105
	v_mul_f32_e32 v0, v110, v0
	v_mul_f32_e32 v8, v111, v8
	v_rcp_f32_e32 v9, v9
	v_rcp_f32_e32 v10, v10
	v_add_f32_e32 v11, 1.0, v11
	v_add_f32_e32 v12, 1.0, v12
	v_exp_f32_e32 v13, v13
	v_exp_f32_e32 v14, v14
	v_mul_f32_e32 v0, v106, v0
	v_mul_f32_e32 v8, v107, v8
	v_rcp_f32_e32 v11, v11
	v_rcp_f32_e32 v12, v12
	v_or_b32_e32 v6, 48, v6
	v_med3_f32 v0, v0, s19, v229
	v_med3_f32 v15, v8, s19, v229
	v_mov_b32_e32 v8, v1
	v_ashrrev_i32_e32 v7, 31, v6
	v_cvt_pk_fp8_f32 v8, v0, v15
	v_lshlrev_b64 v[6:7], 9, v[6:7]
	v_mul_f32_e32 v9, v112, v9
	v_mul_f32_e32 v10, v113, v10
	v_add_f32_e32 v13, 1.0, v13
	v_add_f32_e32 v14, 1.0, v14
	v_lshl_add_u64 v[6:7], s[46:47], 0, v[6:7]
	v_mul_f32_e32 v9, v108, v9
	v_mul_f32_e32 v10, v109, v10
	v_mul_f32_e32 v11, v102, v11
	v_mul_f32_e32 v12, v103, v12
	v_rcp_f32_e32 v13, v13
	v_rcp_f32_e32 v14, v14
	v_mul_f32_e32 v11, v98, v11
	v_mul_f32_e32 v12, v99, v12
	v_lshl_add_u64 v[4:5], v[6:7], 0, v[4:5]
	v_med3_f32 v0, v9, s19, v229
	v_med3_f32 v6, v10, s19, v229
	v_cvt_pk_fp8_f32 v8, v0, v6 op_sel:[0,0,1]
	v_med3_f32 v0, v11, s19, v229
	v_med3_f32 v6, v12, s19, v229
	v_mov_b32_e32 v9, v1
	v_cvt_pk_fp8_f32 v9, v0, v6
	v_mul_f32_e32 v13, v104, v13
	v_mul_f32_e32 v14, v105, v14
	v_mul_f32_e32 v10, 0xbfb8aa3b, v95
	v_mul_f32_e32 v13, v100, v13
	v_mul_f32_e32 v14, v101, v14
	v_exp_f32_e32 v10, v10
	v_med3_f32 v0, v13, s19, v229
	v_med3_f32 v6, v14, s19, v229
	v_mul_f32_e32 v7, 0xbfb8aa3b, v94
	v_exp_f32_e32 v7, v7
	v_cvt_pk_fp8_f32 v9, v0, v6 op_sel:[0,0,1]
	v_add_f32_e32 v6, 1.0, v10
	v_rcp_f32_e32 v6, v6
	v_add_f32_e32 v0, 1.0, v7
	global_store_dwordx2 v[4:5], v[8:9], off
	v_mul_f32_e32 v5, 0xbfb8aa3b, v96
	v_mul_f32_e32 v7, 0xbfb8aa3b, v86
	v_mul_f32_e32 v8, 0xbfb8aa3b, v87
	v_exp_f32_e32 v5, v5
	v_exp_f32_e32 v7, v7
	v_exp_f32_e32 v8, v8
	v_mul_f32_e32 v4, v95, v6
	v_mul_f32_e32 v6, 0xbfb8aa3b, v97
	v_exp_f32_e32 v6, v6
	v_mul_f32_e32 v9, 0xbfb8aa3b, v88
	v_mul_f32_e32 v10, 0xbfb8aa3b, v89
	v_rcp_f32_e32 v0, v0
	v_add_f32_e32 v5, 1.0, v5
	v_add_f32_e32 v7, 1.0, v7
	v_add_f32_e32 v8, 1.0, v8
	v_exp_f32_e32 v9, v9
	v_exp_f32_e32 v10, v10
	v_rcp_f32_e32 v5, v5
	v_rcp_f32_e32 v7, v7
	v_rcp_f32_e32 v8, v8
	v_add_f32_e32 v6, 1.0, v6
	v_mul_f32_e32 v0, v94, v0
	v_rcp_f32_e32 v6, v6
	v_add_f32_e32 v9, 1.0, v9
	v_add_f32_e32 v10, 1.0, v10
	v_mul_f32_e32 v0, v90, v0
	v_mul_f32_e32 v4, v91, v4
	v_mul_f32_e32 v5, v96, v5
	v_mul_f32_e32 v7, v86, v7
	v_mul_f32_e32 v8, v87, v8
	v_rcp_f32_e32 v9, v9
	v_rcp_f32_e32 v10, v10
	v_mul_f32_e32 v5, v92, v5
	v_mul_f32_e32 v7, v82, v7
	v_mul_f32_e32 v8, v83, v8
	v_med3_f32 v0, v0, s19, v229
	v_med3_f32 v11, v4, s19, v229
	v_mov_b32_e32 v4, v1
	v_cvt_pk_fp8_f32 v4, v0, v11
	v_med3_f32 v0, v5, s19, v229
	v_med3_f32 v7, v7, s19, v229
	v_med3_f32 v8, v8, s19, v229
	v_mov_b32_e32 v5, v1
	v_mul_f32_e32 v6, v97, v6
	v_cvt_pk_fp8_f32 v5, v7, v8
	v_mul_f32_e32 v6, v93, v6
	v_mul_f32_e32 v9, v88, v9
	v_mul_f32_e32 v10, v89, v10
	v_mul_f32_e32 v9, v84, v9
	v_mul_f32_e32 v10, v85, v10
	v_med3_f32 v6, v6, s19, v229
	v_cvt_pk_fp8_f32 v4, v0, v6 op_sel:[0,0,1]
	v_med3_f32 v0, v9, s19, v229
	v_med3_f32 v6, v10, s19, v229
	v_cvt_pk_fp8_f32 v5, v0, v6 op_sel:[0,0,1]
	v_mul_f32_e32 v6, 0xbfb8aa3b, v79
	v_exp_f32_e32 v8, v6
	s_mov_b32 s12, 0x10000
	v_add_co_u32_e32 v6, vcc, s12, v2
	v_add_f32_e32 v8, 1.0, v8
	v_rcp_f32_e32 v8, v8
	v_mul_f32_e32 v0, 0xbfb8aa3b, v78
	v_addc_co_u32_e32 v7, vcc, 0, v3, vcc
	v_exp_f32_e32 v0, v0
	global_store_dwordx2 v[6:7], v[4:5], off
	v_mul_f32_e32 v4, v79, v8
	v_mul_f32_e32 v5, 0xbfb8aa3b, v80
	v_mul_f32_e32 v7, 0xbfb8aa3b, v70
	v_mul_f32_e32 v8, 0xbfb8aa3b, v71
	v_exp_f32_e32 v5, v5
	v_exp_f32_e32 v7, v7
	v_exp_f32_e32 v8, v8
	v_mul_f32_e32 v6, 0xbfb8aa3b, v81
	v_add_f32_e32 v0, 1.0, v0
	v_exp_f32_e32 v6, v6
	v_mul_f32_e32 v9, 0xbfb8aa3b, v72
	v_mul_f32_e32 v10, 0xbfb8aa3b, v73
	v_rcp_f32_e32 v0, v0
	v_add_f32_e32 v5, 1.0, v5
	v_add_f32_e32 v7, 1.0, v7
	v_add_f32_e32 v8, 1.0, v8
	v_exp_f32_e32 v9, v9
	v_exp_f32_e32 v10, v10
	v_rcp_f32_e32 v5, v5
	v_rcp_f32_e32 v7, v7
	v_rcp_f32_e32 v8, v8
	v_add_f32_e32 v6, 1.0, v6
	v_mul_f32_e32 v0, v78, v0
	v_rcp_f32_e32 v6, v6
	v_add_f32_e32 v9, 1.0, v9
	v_add_f32_e32 v10, 1.0, v10
	v_mul_f32_e32 v0, v74, v0
	v_mul_f32_e32 v4, v75, v4
	v_mul_f32_e32 v5, v80, v5
	v_mul_f32_e32 v7, v70, v7
	v_mul_f32_e32 v8, v71, v8
	v_rcp_f32_e32 v9, v9
	v_rcp_f32_e32 v10, v10
	v_mul_f32_e32 v5, v76, v5
	v_mul_f32_e32 v7, v66, v7
	v_mul_f32_e32 v8, v67, v8
	v_med3_f32 v0, v0, s19, v229
	v_med3_f32 v11, v4, s19, v229
	v_mov_b32_e32 v4, v1
	v_cvt_pk_fp8_f32 v4, v0, v11
	v_med3_f32 v0, v5, s19, v229
	v_med3_f32 v7, v7, s19, v229
	v_med3_f32 v8, v8, s19, v229
	v_mov_b32_e32 v5, v1
	v_mul_f32_e32 v6, v81, v6
	v_cvt_pk_fp8_f32 v5, v7, v8
	v_mul_f32_e32 v6, v77, v6
	v_mul_f32_e32 v9, v72, v9
	v_mul_f32_e32 v10, v73, v10
	v_mul_f32_e32 v9, v68, v9
	v_mul_f32_e32 v10, v69, v10
	v_med3_f32 v6, v6, s19, v229
	v_cvt_pk_fp8_f32 v4, v0, v6 op_sel:[0,0,1]
	v_med3_f32 v0, v9, s19, v229
	v_med3_f32 v6, v10, s19, v229
	v_cvt_pk_fp8_f32 v5, v0, v6 op_sel:[0,0,1]
	v_mul_f32_e32 v6, 0xbfb8aa3b, v63
	v_exp_f32_e32 v8, v6
	s_mov_b32 s12, 0x12000
	v_add_co_u32_e32 v6, vcc, s12, v2
	v_add_f32_e32 v8, 1.0, v8
	v_rcp_f32_e32 v8, v8
	v_mul_f32_e32 v0, 0xbfb8aa3b, v62
	v_addc_co_u32_e32 v7, vcc, 0, v3, vcc
	v_exp_f32_e32 v0, v0
	global_store_dwordx2 v[6:7], v[4:5], off
	v_mul_f32_e32 v4, v63, v8
	v_mul_f32_e32 v5, 0xbfb8aa3b, v64
	v_mul_f32_e32 v7, 0xbfb8aa3b, v54
	v_mul_f32_e32 v8, 0xbfb8aa3b, v55
	v_exp_f32_e32 v5, v5
	v_exp_f32_e32 v7, v7
	v_exp_f32_e32 v8, v8
	v_mul_f32_e32 v6, 0xbfb8aa3b, v65
	v_add_f32_e32 v0, 1.0, v0
	v_exp_f32_e32 v6, v6
	v_mul_f32_e32 v9, 0xbfb8aa3b, v56
	v_mul_f32_e32 v10, 0xbfb8aa3b, v57
	v_rcp_f32_e32 v0, v0
	v_add_f32_e32 v5, 1.0, v5
	v_add_f32_e32 v7, 1.0, v7
	v_add_f32_e32 v8, 1.0, v8
	v_exp_f32_e32 v9, v9
	v_exp_f32_e32 v10, v10
	v_rcp_f32_e32 v5, v5
	v_rcp_f32_e32 v7, v7
	v_rcp_f32_e32 v8, v8
	v_add_f32_e32 v6, 1.0, v6
	v_mul_f32_e32 v0, v62, v0
	v_rcp_f32_e32 v6, v6
	v_add_f32_e32 v9, 1.0, v9
	v_add_f32_e32 v10, 1.0, v10
	v_mul_f32_e32 v0, v58, v0
	v_mul_f32_e32 v4, v59, v4
	v_mul_f32_e32 v5, v64, v5
	v_mul_f32_e32 v7, v54, v7
	v_mul_f32_e32 v8, v55, v8
	v_rcp_f32_e32 v9, v9
	v_rcp_f32_e32 v10, v10
	v_mul_f32_e32 v5, v60, v5
	v_mul_f32_e32 v7, v50, v7
	v_mul_f32_e32 v8, v51, v8
	v_med3_f32 v0, v0, s19, v229
	v_med3_f32 v11, v4, s19, v229
	v_mov_b32_e32 v4, v1
	v_cvt_pk_fp8_f32 v4, v0, v11
	v_med3_f32 v0, v5, s19, v229
	v_med3_f32 v7, v7, s19, v229
	v_med3_f32 v8, v8, s19, v229
	v_mov_b32_e32 v5, v1
	v_mul_f32_e32 v6, v65, v6
	v_cvt_pk_fp8_f32 v5, v7, v8
	v_mul_f32_e32 v6, v61, v6
	v_mul_f32_e32 v9, v56, v9
	v_mul_f32_e32 v10, v57, v10
	v_mul_f32_e32 v9, v52, v9
	v_mul_f32_e32 v10, v53, v10
	v_med3_f32 v6, v6, s19, v229
	v_cvt_pk_fp8_f32 v4, v0, v6 op_sel:[0,0,1]
	v_med3_f32 v0, v9, s19, v229
	v_med3_f32 v6, v10, s19, v229
	v_cvt_pk_fp8_f32 v5, v0, v6 op_sel:[0,0,1]
	v_mul_f32_e32 v6, 0xbfb8aa3b, v47
	v_exp_f32_e32 v8, v6
	s_mov_b32 s12, 0x14000
	v_add_co_u32_e32 v6, vcc, s12, v2
	v_add_f32_e32 v8, 1.0, v8
	v_rcp_f32_e32 v8, v8
	v_mul_f32_e32 v0, 0xbfb8aa3b, v46
	v_addc_co_u32_e32 v7, vcc, 0, v3, vcc
	v_exp_f32_e32 v0, v0
	global_store_dwordx2 v[6:7], v[4:5], off
	v_mul_f32_e32 v4, v47, v8
	v_mul_f32_e32 v5, 0xbfb8aa3b, v48
	v_mul_f32_e32 v7, 0xbfb8aa3b, v38
	v_mul_f32_e32 v8, 0xbfb8aa3b, v39
	v_exp_f32_e32 v5, v5
	v_exp_f32_e32 v7, v7
	v_exp_f32_e32 v8, v8
	v_mul_f32_e32 v6, 0xbfb8aa3b, v49
	v_add_f32_e32 v0, 1.0, v0
	v_exp_f32_e32 v6, v6
	v_mul_f32_e32 v9, 0xbfb8aa3b, v40
	v_mul_f32_e32 v10, 0xbfb8aa3b, v41
	v_rcp_f32_e32 v0, v0
	v_add_f32_e32 v5, 1.0, v5
	v_add_f32_e32 v7, 1.0, v7
	v_add_f32_e32 v8, 1.0, v8
	v_exp_f32_e32 v9, v9
	v_exp_f32_e32 v10, v10
	v_rcp_f32_e32 v5, v5
	v_rcp_f32_e32 v7, v7
	v_rcp_f32_e32 v8, v8
	v_add_f32_e32 v6, 1.0, v6
	v_mul_f32_e32 v0, v46, v0
	v_rcp_f32_e32 v6, v6
	v_add_f32_e32 v9, 1.0, v9
	v_add_f32_e32 v10, 1.0, v10
	v_mul_f32_e32 v0, v42, v0
	v_mul_f32_e32 v4, v43, v4
	v_mul_f32_e32 v5, v48, v5
	v_mul_f32_e32 v7, v38, v7
	v_mul_f32_e32 v8, v39, v8
	v_rcp_f32_e32 v9, v9
	v_rcp_f32_e32 v10, v10
	v_mul_f32_e32 v5, v44, v5
	v_mul_f32_e32 v7, v34, v7
	v_mul_f32_e32 v8, v35, v8
	v_med3_f32 v0, v0, s19, v229
	v_med3_f32 v11, v4, s19, v229
	v_mov_b32_e32 v4, v1
	v_cvt_pk_fp8_f32 v4, v0, v11
	v_med3_f32 v0, v5, s19, v229
	v_med3_f32 v7, v7, s19, v229
	v_med3_f32 v8, v8, s19, v229
	v_mov_b32_e32 v5, v1
	v_mul_f32_e32 v6, v49, v6
	v_cvt_pk_fp8_f32 v5, v7, v8
	v_mul_f32_e32 v6, v45, v6
	v_mul_f32_e32 v9, v40, v9
	v_mul_f32_e32 v10, v41, v10
	v_mul_f32_e32 v9, v36, v9
	v_mul_f32_e32 v10, v37, v10
	v_med3_f32 v6, v6, s19, v229
	v_cvt_pk_fp8_f32 v4, v0, v6 op_sel:[0,0,1]
	v_med3_f32 v0, v9, s19, v229
	v_med3_f32 v6, v10, s19, v229
	v_cvt_pk_fp8_f32 v5, v0, v6 op_sel:[0,0,1]
	v_add_co_u32_e32 v2, vcc, 0x16000, v2
	s_nop 1
	v_addc_co_u32_e32 v3, vcc, 0, v3, vcc
	s_and_b64 vcc, exec, s[38:39]
	s_mov_b64 s[38:39], -1
	global_store_dwordx2 v[2:3], v[4:5], off
	s_cbranch_vccnz .LBB0_1185
	s_andn2_b64 vcc, exec, s[44:45]
	s_cbranch_vccnz .LBB0_1184
	s_barrier
	s_branch .LBB0_1184

.LBB0_1293:
	s_ashr_i32 s54, s79, 31
	s_lshr_b32 s54, s54, 29
	s_add_i32 s54, s79, s54
	s_and_b32 s54, s54, 0xfffff8
	v_mov_b32_e32 v34, v181
	s_sub_i32 s54, s79, s54
	s_lshl_b32 s55, s78, 8
	v_readlane_b32 s100, v252, 5
	s_cmp_ge_u32 s100, 4
	s_cbranch_scc0 .Lepi_prio_5
	s_setprio 1
.Lepi_prio_5:
	s_nop 15
	s_nop 15
	s_add_i32 s55, s55, s69
	s_lshl_b32 s54, s54, 8
	v_and_or_b32 v40, v34, 15, s55
	v_and_b32_e32 v34, -16, v34
	s_or_b32 s54, s54, s73
	v_add_u32_e32 v44, s54, v34
	v_med3_f32 v34, v158, s19, v229
	v_med3_f32 v35, v159, s19, v229
	v_mov_b32_e32 v36, v1
	v_cvt_pk_fp8_f32 v36, v34, v35
	v_med3_f32 v38, v154, s19, v229
	v_med3_f32 v39, v155, s19, v229
	v_mov_b32_e32 v37, v1
	v_cvt_pk_fp8_f32 v37, v38, v39
	v_med3_f32 v34, v160, s19, v229
	v_med3_f32 v35, v161, s19, v229
	v_cvt_pk_fp8_f32 v36, v34, v35 op_sel:[0,0,1]
	v_med3_f32 v34, v156, s19, v229
	v_med3_f32 v35, v157, s19, v229
	v_cvt_pk_fp8_f32 v37, v34, v35 op_sel:[0,0,1]
	v_med3_f32 v34, v172, s19, v229
	v_med3_f32 v35, v173, s19, v229
	v_mov_b32_e32 v38, v1
	v_cvt_pk_fp8_f32 v38, v34, v35
	v_med3_f32 v48, v174, s19, v229
	v_med3_f32 v49, v175, s19, v229
	v_mov_b32_e32 v39, v1
	v_cvt_pk_fp8_f32 v39, v48, v49
	v_med3_f32 v34, v170, s19, v229
	v_med3_f32 v35, v171, s19, v229
	v_cvt_pk_fp8_f32 v38, v34, v35 op_sel:[0,0,1]
	v_med3_f32 v34, v168, s19, v229
	v_med3_f32 v35, v169, s19, v229
	v_ashrrev_i32_e32 v41, 31, v40
	v_cvt_pk_fp8_f32 v39, v34, v35 op_sel:[0,0,1]
	v_lshlrev_b64 v[34:35], 11, v[40:41]
	v_ashrrev_i32_e32 v45, 31, v44
	v_lshl_add_u64 v[34:35], s[44:45], 0, v[34:35]
	v_lshl_add_u64 v[34:35], v[34:35], 0, v[44:45]
	global_store_dwordx4 v[34:35], v[36:39], off
	v_med3_f32 v41, v144, s19, v229
	v_med3_f32 v50, v145, s19, v229
	v_med3_f32 v37, v142, s19, v229
	v_med3_f32 v38, v143, s19, v229
	v_mov_b32_e32 v36, v1
	v_cvt_pk_fp8_f32 v36, v37, v38
	v_mov_b32_e32 v37, v1
	v_cvt_pk_fp8_f32 v37, v41, v50
	v_med3_f32 v38, v136, s19, v229
	v_med3_f32 v39, v137, s19, v229
	v_cvt_pk_fp8_f32 v36, v38, v39 op_sel:[0,0,1]
	v_med3_f32 v38, v134, s19, v229
	v_med3_f32 v39, v135, s19, v229
	v_cvt_pk_fp8_f32 v37, v38, v39 op_sel:[0,0,1]
	v_med3_f32 v39, v150, s19, v229
	v_med3_f32 v41, v151, s19, v229
	v_mov_b32_e32 v38, v1
	v_cvt_pk_fp8_f32 v38, v39, v41
	v_med3_f32 v51, v152, s19, v229
	v_med3_f32 v52, v153, s19, v229
	v_mov_b32_e32 v39, v1
	v_cvt_pk_fp8_f32 v39, v51, v52
	v_med3_f32 v41, v148, s19, v229
	v_med3_f32 v50, v149, s19, v229
	v_or_b32_e32 v48, 16, v40
	v_cvt_pk_fp8_f32 v38, v41, v50 op_sel:[0,0,1]
	v_med3_f32 v41, v146, s19, v229
	v_med3_f32 v50, v147, s19, v229
	v_ashrrev_i32_e32 v49, 31, v48
	v_cvt_pk_fp8_f32 v39, v41, v50 op_sel:[0,0,1]
	v_lshlrev_b64 v[48:49], 11, v[48:49]
	v_lshl_add_u64 v[48:49], s[44:45], 0, v[48:49]
	v_lshl_add_u64 v[48:49], v[48:49], 0, v[44:45]
	global_store_dwordx4 v[48:49], v[36:39], off
	v_med3_f32 v41, v128, s19, v229
	v_med3_f32 v50, v129, s19, v229
	v_med3_f32 v37, v126, s19, v229
	v_med3_f32 v38, v127, s19, v229
	v_mov_b32_e32 v36, v1
	v_cvt_pk_fp8_f32 v36, v37, v38
	v_mov_b32_e32 v37, v1
	v_cvt_pk_fp8_f32 v37, v41, v50
	v_med3_f32 v38, v120, s19, v229
	v_med3_f32 v39, v121, s19, v229
	v_cvt_pk_fp8_f32 v36, v38, v39 op_sel:[0,0,1]
	v_med3_f32 v38, v118, s19, v229
	v_med3_f32 v39, v119, s19, v229
	v_cvt_pk_fp8_f32 v37, v38, v39 op_sel:[0,0,1]
	v_med3_f32 v39, v138, s19, v229
	v_med3_f32 v41, v139, s19, v229
	v_mov_b32_e32 v38, v1
	v_cvt_pk_fp8_f32 v38, v39, v41
	v_med3_f32 v51, v140, s19, v229
	v_med3_f32 v52, v141, s19, v229
	v_mov_b32_e32 v39, v1
	v_cvt_pk_fp8_f32 v39, v51, v52
	v_med3_f32 v41, v132, s19, v229
	v_med3_f32 v50, v133, s19, v229
	v_or_b32_e32 v48, 32, v40
	v_cvt_pk_fp8_f32 v38, v41, v50 op_sel:[0,0,1]
	v_med3_f32 v41, v130, s19, v229
	v_med3_f32 v50, v131, s19, v229
	v_ashrrev_i32_e32 v49, 31, v48
	v_cvt_pk_fp8_f32 v39, v41, v50 op_sel:[0,0,1]
	v_lshlrev_b64 v[48:49], 11, v[48:49]
	v_lshl_add_u64 v[48:49], s[44:45], 0, v[48:49]
	v_lshl_add_u64 v[48:49], v[48:49], 0, v[44:45]
	global_store_dwordx4 v[48:49], v[36:39], off
	v_med3_f32 v48, v112, s19, v229
	v_med3_f32 v49, v113, s19, v229
	v_med3_f32 v37, v110, s19, v229
	v_med3_f32 v38, v111, s19, v229
	v_mov_b32_e32 v36, v1
	v_cvt_pk_fp8_f32 v36, v37, v38
	v_mov_b32_e32 v37, v1
	v_cvt_pk_fp8_f32 v37, v48, v49
	v_med3_f32 v38, v108, s19, v229
	v_med3_f32 v39, v109, s19, v229
	v_cvt_pk_fp8_f32 v36, v38, v39 op_sel:[0,0,1]
	v_med3_f32 v38, v106, s19, v229
	v_med3_f32 v39, v107, s19, v229
	v_cvt_pk_fp8_f32 v37, v38, v39 op_sel:[0,0,1]
	v_med3_f32 v39, v102, s19, v229
	v_med3_f32 v48, v103, s19, v229
	v_mov_b32_e32 v38, v1
	v_cvt_pk_fp8_f32 v38, v39, v48
	v_med3_f32 v50, v98, s19, v229
	v_med3_f32 v51, v99, s19, v229
	v_mov_b32_e32 v39, v1
	v_cvt_pk_fp8_f32 v39, v50, v51
	v_med3_f32 v48, v104, s19, v229
	v_med3_f32 v49, v105, s19, v229
	v_or_b32_e32 v40, 48, v40
	v_cvt_pk_fp8_f32 v38, v48, v49 op_sel:[0,0,1]
	v_med3_f32 v48, v100, s19, v229
	v_med3_f32 v49, v101, s19, v229
	v_ashrrev_i32_e32 v41, 31, v40
	v_cvt_pk_fp8_f32 v39, v48, v49 op_sel:[0,0,1]
	v_lshlrev_b64 v[40:41], 11, v[40:41]
	v_lshl_add_u64 v[40:41], s[44:45], 0, v[40:41]
	v_lshl_add_u64 v[40:41], v[40:41], 0, v[44:45]
	global_store_dwordx4 v[40:41], v[36:39], off
	v_med3_f32 v40, v90, s19, v229
	v_med3_f32 v41, v91, s19, v229
	v_med3_f32 v37, v94, s19, v229
	v_med3_f32 v38, v95, s19, v229
	v_mov_b32_e32 v36, v1
	v_cvt_pk_fp8_f32 v36, v37, v38
	v_mov_b32_e32 v37, v1
	v_cvt_pk_fp8_f32 v37, v40, v41
	v_med3_f32 v38, v96, s19, v229
	v_med3_f32 v39, v97, s19, v229
	v_cvt_pk_fp8_f32 v36, v38, v39 op_sel:[0,0,1]
	v_med3_f32 v38, v92, s19, v229
	v_med3_f32 v39, v93, s19, v229
	v_cvt_pk_fp8_f32 v37, v38, v39 op_sel:[0,0,1]
	v_med3_f32 v39, v114, s19, v229
	v_med3_f32 v40, v115, s19, v229
	v_mov_b32_e32 v38, v1
	v_cvt_pk_fp8_f32 v38, v39, v40
	v_med3_f32 v44, v116, s19, v229
	v_med3_f32 v45, v117, s19, v229
	v_mov_b32_e32 v39, v1
	v_cvt_pk_fp8_f32 v39, v44, v45
	v_med3_f32 v40, v80, s19, v229
	v_med3_f32 v41, v81, s19, v229
	v_cvt_pk_fp8_f32 v38, v40, v41 op_sel:[0,0,1]
	v_med3_f32 v40, v78, s19, v229
	v_med3_f32 v41, v79, s19, v229
	v_cvt_pk_fp8_f32 v39, v40, v41 op_sel:[0,0,1]
	s_mov_b32 s54, 0x40000
	v_add_co_u32_e32 v40, vcc, s54, v34
	v_med3_f32 v26, v26, s19, v229
	s_nop 0
	v_addc_co_u32_e32 v41, vcc, 0, v35, vcc
	global_store_dwordx4 v[40:41], v[36:39], off
	v_med3_f32 v27, v27, s19, v229
	v_med3_f32 v28, v28, s19, v229
	v_med3_f32 v37, v70, s19, v229
	v_med3_f32 v38, v71, s19, v229
	v_mov_b32_e32 v36, v1
	v_cvt_pk_fp8_f32 v36, v37, v38
	v_med3_f32 v38, v72, s19, v229
	v_med3_f32 v39, v73, s19, v229
	v_mov_b32_e32 v37, v1
	v_cvt_pk_fp8_f32 v37, v38, v39
	v_med3_f32 v29, v29, s19, v229
	v_mov_b32_e32 v38, v1
	v_cvt_pk_fp8_f32 v36, v28, v29 op_sel:[0,0,1]
	v_cvt_pk_fp8_f32 v37, v26, v27 op_sel:[0,0,1]
	v_med3_f32 v26, v62, s19, v229
	v_med3_f32 v27, v63, s19, v229
	v_cvt_pk_fp8_f32 v38, v26, v27
	v_med3_f32 v28, v54, s19, v229
	v_med3_f32 v29, v55, s19, v229
	v_mov_b32_e32 v39, v1
	v_cvt_pk_fp8_f32 v39, v28, v29
	v_med3_f32 v26, v64, s19, v229
	v_med3_f32 v27, v65, s19, v229
	v_cvt_pk_fp8_f32 v38, v26, v27 op_sel:[0,0,1]
	v_med3_f32 v26, v56, s19, v229
	v_med3_f32 v27, v57, s19, v229
	v_cvt_pk_fp8_f32 v39, v26, v27 op_sel:[0,0,1]
	s_mov_b32 s54, 0x48000
	v_add_co_u32_e32 v26, vcc, s54, v34
	v_med3_f32 v19, v19, s19, v229
	s_nop 0
	v_addc_co_u32_e32 v27, vcc, 0, v35, vcc
	global_store_dwordx4 v[26:27], v[36:39], off
	v_med3_f32 v26, v18, s19, v229
	v_mov_b32_e32 v18, v1
	v_cvt_pk_fp8_f32 v18, v26, v19
	v_med3_f32 v20, v20, s19, v229
	v_med3_f32 v21, v21, s19, v229
	v_mov_b32_e32 v19, v1
	v_cvt_pk_fp8_f32 v19, v20, v21
	v_med3_f32 v10, v10, s19, v229
	v_med3_f32 v11, v11, s19, v229
	v_med3_f32 v12, v12, s19, v229
	v_med3_f32 v13, v13, s19, v229
	v_cvt_pk_fp8_f32 v19, v10, v11 op_sel:[0,0,1]
	v_med3_f32 v10, v46, s19, v229
	v_med3_f32 v11, v47, s19, v229
	v_mov_b32_e32 v20, v1
	v_cvt_pk_fp8_f32 v18, v12, v13 op_sel:[0,0,1]
	v_cvt_pk_fp8_f32 v20, v10, v11
	v_med3_f32 v12, v42, s19, v229
	v_med3_f32 v13, v43, s19, v229
	v_mov_b32_e32 v21, v1
	v_cvt_pk_fp8_f32 v21, v12, v13
	v_med3_f32 v10, v32, s19, v229
	v_med3_f32 v11, v33, s19, v229
	v_cvt_pk_fp8_f32 v20, v10, v11 op_sel:[0,0,1]
	v_med3_f32 v10, v30, s19, v229
	v_med3_f32 v11, v31, s19, v229
	v_cvt_pk_fp8_f32 v21, v10, v11 op_sel:[0,0,1]
	s_mov_b32 s54, 0x50000
	v_add_co_u32_e32 v10, vcc, s54, v34
	v_med3_f32 v7, v7, s19, v229
	s_nop 0
	v_addc_co_u32_e32 v11, vcc, 0, v35, vcc
	global_store_dwordx4 v[10:11], v[18:21], off
	v_med3_f32 v10, v6, s19, v229
	v_mov_b32_e32 v6, v1
	v_cvt_pk_fp8_f32 v6, v10, v7
	v_med3_f32 v8, v8, s19, v229
	v_med3_f32 v9, v9, s19, v229
	v_mov_b32_e32 v7, v1
	v_cvt_pk_fp8_f32 v7, v8, v9
	v_med3_f32 v2, v2, s19, v229
	v_med3_f32 v3, v3, s19, v229
	v_med3_f32 v4, v4, s19, v229
	v_med3_f32 v5, v5, s19, v229
	v_cvt_pk_fp8_f32 v7, v2, v3 op_sel:[0,0,1]
	v_med3_f32 v2, v22, s19, v229
	v_med3_f32 v3, v23, s19, v229
	v_mov_b32_e32 v8, v1
	v_cvt_pk_fp8_f32 v6, v4, v5 op_sel:[0,0,1]
	v_cvt_pk_fp8_f32 v8, v2, v3
	v_med3_f32 v4, v24, s19, v229
	v_med3_f32 v5, v25, s19, v229
	v_mov_b32_e32 v9, v1
	v_cvt_pk_fp8_f32 v9, v4, v5
	v_med3_f32 v2, v16, s19, v229
	v_med3_f32 v3, v17, s19, v229
	v_cvt_pk_fp8_f32 v8, v2, v3 op_sel:[0,0,1]
	v_med3_f32 v2, v14, s19, v229
	v_med3_f32 v3, v15, s19, v229
	v_cvt_pk_fp8_f32 v9, v2, v3 op_sel:[0,0,1]
	v_add_co_u32_e32 v2, vcc, 0x58000, v34
	s_nop 1
	v_addc_co_u32_e32 v3, vcc, 0, v35, vcc
	s_and_b64 vcc, exec, s[38:39]
	s_mov_b64 s[38:39], -1
	global_store_dwordx4 v[2:3], v[6:9], off
	s_cbranch_vccnz .LBB0_1277
	s_andn2_b64 vcc, exec, s[42:43]
	s_cbranch_vccnz .LBB0_1276
	s_barrier
	s_branch .LBB0_1276
